# P8 gate math: EXEC save/restore of the rare exact-expm1 fix-up moved into the stubs (fast path: s_and_b64 vcc + s_cbranch_vccnz, no EXEC writes), 32 sites per unit
# speedup vs baseline: 1.0060x; 1.0060x over previous
.LBB0_1262:
	s_mov_b32 s98, 0x3fb17218
	s_mul_hi_i32 s20, s80, 0x66666667
	s_lshr_b32 s48, s20, 31
	s_ashr_i32 s20, s20, 2
	s_add_i32 s20, s20, s48
	s_mul_i32 s48, s20, 0xfffffb00
	s_add_i32 s48, s48, s35
	s_waitcnt lgkmcnt(0)
	v_add_u32_e32 v2, s48, v158
	v_ashrrev_i32_e32 v3, 31, v2
	v_lshlrev_b64 v[2:3], 2, v[2:3]
	v_lshl_add_u64 v[6:7], s[62:63], 0, v[2:3]
	v_add_co_u32_e32 v4, vcc, s3, v6
	global_load_dwordx4 v[58:61], v[6:7], off
	s_nop 0
	v_addc_co_u32_e32 v5, vcc, 0, v7, vcc
	global_load_dwordx4 v[94:97], v[4:5], off offset:1024
	v_lshl_add_u64 v[2:3], s[64:65], 0, v[2:3]
	global_load_dwordx4 v[70:73], v[2:3], off
	v_lshl_add_u64 v[4:5], v[6:7], 0, s[38:39]
	global_load_dwordx4 v[98:101], v[4:5], off offset:16
	global_load_dwordx4 v[62:65], v[6:7], off offset:16
	global_load_dwordx4 v[66:69], v[2:3], off offset:16
	s_mul_i32 s52, s20, 0xffffffec
	v_add_co_u32_e32 v2, vcc, s29, v6
	s_add_i32 s52, s33, s52
	s_nop 0
	v_addc_co_u32_e32 v3, vcc, 0, v7, vcc
	s_ashr_i32 s53, s52, 31
	v_add_co_u32_e32 v4, vcc, s47, v6
	s_lshl_b64 s[54:55], s[52:53], 16
	s_nop 0
	v_addc_co_u32_e32 v5, vcc, 0, v7, vcc
	v_lshl_add_u64 v[8:9], v[156:157], 0, s[54:55]
	global_load_dwordx4 v[102:105], v[4:5], off offset:3072
	global_load_dwordx4 v[86:89], v[2:3], off offset:2048
	global_load_dwordx4 v[42:45], v[8:9], off
	global_load_dwordx4 v[26:29], v[8:9], off offset:1024
	global_load_dwordx4 v[10:13], v[8:9], off offset:2048
	s_nop 0
	global_load_dwordx4 v[2:5], v[8:9], off offset:3072
	v_add_co_u32_e32 v22, vcc, s3, v8
	v_lshlrev_b32_e32 v111, 16, v201
	s_nop 0
	v_addc_co_u32_e32 v23, vcc, 0, v9, vcc
	v_add_co_u32_e32 v24, vcc, s29, v8
	v_lshlrev_b32_e32 v110, 16, v206
	s_nop 0
	v_addc_co_u32_e32 v25, vcc, 0, v9, vcc
	v_add_co_u32_e32 v82, vcc, s47, v8
	global_load_dwordx4 v[30:33], v[22:23], off offset:1024
	global_load_dwordx4 v[14:17], v[22:23], off offset:2048
	global_load_dwordx4 v[46:49], v[24:25], off offset:-4096
	global_load_dwordx4 v[50:53], v[24:25], off
	global_load_dwordx4 v[34:37], v[24:25], off offset:1024
	global_load_dwordx4 v[18:21], v[24:25], off offset:2048
	v_addc_co_u32_e32 v83, vcc, 0, v9, vcc
	v_lshl_add_u64 v[8:9], v[6:7], 0, s[40:41]
	v_lshl_add_u64 v[6:7], v[6:7], 0, s[42:43]
	global_load_dwordx4 v[106:109], v[6:7], off offset:16
	global_load_dwordx4 v[74:77], v[8:9], off offset:16
	global_load_dwordx4 v[78:81], v[24:25], off offset:3072
	s_nop 0
	global_load_dwordx4 v[6:9], v[22:23], off offset:3072
	global_load_dwordx4 v[54:57], v[82:83], off
	global_load_dwordx4 v[38:41], v[82:83], off offset:1024
	s_nop 0
	global_load_dwordx4 v[22:25], v[82:83], off offset:2048
	s_nop 0
	global_load_dwordx4 v[82:85], v[82:83], off offset:3072
	v_lshlrev_b32_e32 v114, 16, v207
	v_lshlrev_b32_e32 v115, 16, v202
	v_and_b32_e32 v117, 0xffff0000, v202
	v_and_b32_e32 v116, 0xffff0000, v207
	v_and_b32_e32 v113, 0xffff0000, v201
	v_and_b32_e32 v112, 0xffff0000, v206
	v_and_b32_e32 v121, 0xffff0000, v203
	v_and_b32_e32 v120, 0xffff0000, v209
	v_lshlrev_b32_e32 v122, 16, v210
	v_lshlrev_b32_e32 v123, 16, v205
	v_and_b32_e32 v125, 0xffff0000, v205
	v_and_b32_e32 v124, 0xffff0000, v210
	v_lshlrev_b32_e32 v127, 16, v212
	v_lshlrev_b32_e32 v126, 16, v218
	v_and_b32_e32 v129, 0xffff0000, v212
	v_and_b32_e32 v128, 0xffff0000, v218
	v_lshlrev_b32_e32 v131, 16, v213
	v_and_b32_e32 v133, 0xffff0000, v213
	v_and_b32_e32 v132, 0xffff0000, v219
	v_lshlrev_b32_e32 v135, 16, v215
	v_and_b32_e32 v137, 0xffff0000, v215
	v_and_b32_e32 v136, 0xffff0000, v221
	v_lshlrev_b32_e32 v139, 16, v216
	v_and_b32_e32 v141, 0xffff0000, v216
	v_and_b32_e32 v140, 0xffff0000, v222
	s_and_b32 s49, s79, 0x8000
	s_add_i32 s49, s49, 0
	v_add3_u32 v147, s49, v186, v187
	s_add_i32 s53, s31, s49
	s_add_i32 s52, s52, 1
	v_add_u32_e32 v245, s49, v165
	s_waitcnt vmcnt(14)
	v_mov_b32_e32 v93, v58
	v_mov_b32_e32 v91, v60
	v_mov_b32_e32 v92, v94
	v_mov_b32_e32 v58, v95
	v_mov_b32_e32 v90, v96
	v_mov_b32_e32 v60, v97
	v_fma_f32 v95, v93, v111, v70
	v_pk_mul_f32 v[118:119], v[90:91], v[114:115]
	v_fma_f32 v115, v92, v110, v95
	v_add_f32_e32 v111, v119, v72
	v_fma_f32 v95, v61, v117, v73
	v_fma_f32 v97, v59, v113, v71
	v_add_f32_e32 v111, v118, v111
	v_fma_f32 v134, v60, v116, v95
	v_lshlrev_b32_e32 v119, 16, v203
	v_lshlrev_b32_e32 v118, 16, v209
	v_mov_b32_e32 v94, v98
	v_mov_b32_e32 v95, v62
	v_fma_f32 v130, v58, v112, v97
	s_nop 0
	v_fma_f32 v62, v95, v119, v66
	v_fma_f32 v119, v94, v118, v62
	v_mov_b32_e32 v62, v99
	s_nop 0
	v_fma_f32 v97, v63, v121, v67
	v_fma_f32 v138, v62, v120, v97
	v_mov_b32_e32 v96, v100
	v_mov_b32_e32 v97, v64
	s_nop 0
	v_fma_f32 v64, v97, v123, v68
	v_fma_f32 v123, v96, v122, v64
	v_mov_b32_e32 v64, v101
	s_nop 0
	v_fma_f32 v99, v65, v125, v69
	v_fma_f32 v142, v64, v124, v99
	v_mov_b32_e32 v98, v102
	v_mov_b32_e32 v99, v86
	s_nop 0
	v_fma_f32 v86, v99, v127, v115
	v_fma_f32 v115, v98, v126, v86
	v_mov_b32_e32 v86, v103
	s_nop 0
	v_fma_f32 v101, v87, v129, v130
	v_fma_f32 v143, v86, v128, v101
	v_lshlrev_b32_e32 v130, 16, v219
	v_mov_b32_e32 v100, v104
	v_mov_b32_e32 v101, v88
	s_nop 0
	v_fma_f32 v88, v101, v131, v111
	v_fma_f32 v111, v100, v130, v88
	v_mov_b32_e32 v88, v105
	s_nop 0
	v_fma_f32 v103, v89, v133, v134
	v_fma_f32 v144, v88, v132, v103
	v_lshlrev_b32_e32 v134, 16, v221
	s_waitcnt vmcnt(7)
	v_mov_b32_e32 v102, v106
	s_waitcnt vmcnt(6)
	v_mov_b32_e32 v103, v74
	s_nop 0
	v_fma_f32 v74, v103, v135, v119
	v_fma_f32 v119, v102, v134, v74
	v_mov_b32_e32 v74, v107
	s_nop 0
	v_fma_f32 v105, v75, v137, v138
	v_fma_f32 v145, v74, v136, v105
	v_lshlrev_b32_e32 v138, 16, v222
	v_mov_b32_e32 v104, v108
	v_mov_b32_e32 v105, v76
	s_nop 0
	v_fma_f32 v76, v105, v139, v123
	v_fma_f32 v123, v104, v138, v76
	v_mov_b32_e32 v76, v109
	s_nop 0
	v_fma_f32 v107, v77, v141, v142
	v_fma_f32 v109, v76, v140, v107
	v_cvt_pk_bf16_f32 v106, v115, v143
	v_cvt_pk_bf16_f32 v107, v111, v144
	v_add3_u32 v111, s49, v184, v185
	v_cvt_pk_bf16_f32 v108, v119, v145
	v_cvt_pk_bf16_f32 v109, v123, v109
	ds_write_b128 v111, v[106:109]
	v_pk_mov_b32 v[106:107], v[126:127], v[110:111] op_sel:[1,0]
	v_lshlrev_b32_e32 v111, 16, v224
	v_lshlrev_b32_e32 v110, 16, v228
	v_fma_f32 v107, v93, v107, v70
	v_fma_f32 v108, v92, v106, v107
	v_pk_mov_b32 v[106:107], v[128:129], v[112:113] op_sel:[1,0]
	v_pk_mov_b32 v[112:113], v[110:111], v[126:127] op_sel:[1,0]
	s_nop 0
	v_fma_f32 v107, v59, v107, v71
	v_fma_f32 v109, v58, v106, v107
	v_pk_mov_b32 v[106:107], v[130:131], v[114:115] op_sel:[1,0]
	v_and_b32_e32 v115, 0xffff0000, v224
	s_nop 0
	v_fma_f32 v107, v91, v107, v72
	v_fma_f32 v123, v90, v106, v107
	v_pk_mov_b32 v[106:107], v[132:133], v[116:117] op_sel:[1,0]
	s_nop 0
	s_nop 0
	v_fma_f32 v107, v61, v107, v73
	v_fma_f32 v142, v60, v106, v107
	v_pk_mov_b32 v[106:107], v[134:135], v[118:119] op_sel:[1,0]
	s_nop 0
	s_nop 0
	v_fma_f32 v107, v95, v107, v66
	v_fma_f32 v143, v94, v106, v107
	v_pk_mov_b32 v[106:107], v[136:137], v[120:121] op_sel:[1,0]
	s_nop 0
	s_nop 0
	v_fma_f32 v107, v63, v107, v67
	v_fma_f32 v144, v62, v106, v107
	v_pk_mov_b32 v[106:107], v[138:139], v[122:123] op_sel:[1,0]
	s_nop 0
	s_nop 0
	v_fma_f32 v107, v97, v107, v68
	v_fma_f32 v145, v96, v106, v107
	v_pk_mov_b32 v[106:107], v[140:141], v[124:125] op_sel:[1,0]
	s_nop 0
	s_nop 0
	v_fma_f32 v107, v65, v107, v69
	v_fma_f32 v146, v64, v106, v107
	v_pk_mul_f32 v[106:107], v[92:93], v[126:127]
	v_lshlrev_b32_e32 v127, 16, v226
	v_add_f32_e32 v107, v107, v70
	v_add_f32_e32 v114, v106, v107
	v_pk_mul_f32 v[92:93], v[92:93], v[112:113]
	v_fma_f32 v107, v59, v129, v71
	v_fma_f32 v118, v58, v128, v107
	v_add_f32_e32 v70, v93, v70
	v_fma_f32 v107, v91, v131, v72
	v_fma_f32 v122, v90, v130, v107
	v_add_f32_e32 v70, v92, v70
	v_fma_f32 v107, v61, v133, v73
	v_fma_f32 v148, v60, v132, v107
	s_nop 0
	v_fma_f32 v107, v95, v135, v66
	v_fma_f32 v149, v94, v134, v107
	s_nop 0
	v_fma_f32 v107, v63, v137, v67
	v_fma_f32 v150, v62, v136, v107
	s_nop 0
	v_fma_f32 v107, v97, v139, v68
	v_fma_f32 v151, v96, v138, v107
	s_nop 0
	v_fma_f32 v107, v65, v141, v69
	v_fma_f32 v152, v64, v140, v107
	s_nop 0
	v_fma_f32 v107, v99, v113, v108
	v_fma_f32 v119, v98, v112, v107
	s_nop 0
	v_fma_f32 v107, v99, v111, v114
	v_and_b32_e32 v114, 0xffff0000, v228
	v_pk_mov_b32 v[116:117], v[114:115], v[128:129] op_sel:[1,0]
	v_fma_f32 v111, v98, v110, v107
	v_pk_mul_f32 v[58:59], v[58:59], v[116:117]
	v_fma_f32 v107, v87, v117, v109
	v_fma_f32 v106, v86, v116, v107
	v_cvt_pk_bf16_f32 v106, v119, v106
	v_lshlrev_b32_e32 v119, 16, v225
	v_fma_f32 v107, v87, v115, v118
	v_lshlrev_b32_e32 v118, 16, v229
	v_pk_mov_b32 v[120:121], v[118:119], v[130:131] op_sel:[1,0]
	v_fma_f32 v115, v86, v114, v107
	v_and_b32_e32 v131, 0xffff0000, v226
	v_fma_f32 v107, v101, v121, v123
	v_fma_f32 v107, v100, v120, v107
	v_and_b32_e32 v123, 0xffff0000, v225
	v_fma_f32 v109, v101, v119, v122
	v_and_b32_e32 v122, 0xffff0000, v229
	v_pk_mov_b32 v[124:125], v[122:123], v[132:133] op_sel:[1,0]
	v_fma_f32 v119, v100, v118, v109
	v_and_b32_e32 v130, 0xffff0000, v230
	v_fma_f32 v109, v89, v125, v142
	v_fma_f32 v126, v88, v124, v109
	v_cvt_pk_bf16_f32 v107, v107, v126
	v_lshlrev_b32_e32 v126, 16, v230
	v_fma_f32 v109, v89, v123, v148
	v_pk_mov_b32 v[128:129], v[126:127], v[134:135] op_sel:[1,0]
	v_fma_f32 v123, v88, v122, v109
	v_pk_mov_b32 v[132:133], v[130:131], v[136:137] op_sel:[1,0]
	v_fma_f32 v109, v103, v129, v143
	v_fma_f32 v142, v102, v128, v109
	v_add_f32_e32 v59, v59, v71
	v_fma_f32 v109, v103, v127, v149
	v_fma_f32 v127, v102, v126, v109
	v_fma_f32 v109, v75, v133, v144
	v_add_f32_e32 v71, v58, v59
	v_fma_f32 v108, v74, v132, v109
	v_fma_f32 v109, v75, v131, v150
	v_fma_f32 v59, v91, v121, v72
	v_fma_f32 v131, v74, v130, v109
	v_lshlrev_b32_e32 v134, 16, v231
	v_lshlrev_b32_e32 v135, 16, v227
	v_fma_f32 v72, v90, v120, v59
	v_pk_mov_b32 v[136:137], v[134:135], v[138:139] op_sel:[1,0]
	v_fma_f32 v59, v61, v125, v73
	v_fma_f32 v60, v60, v124, v59
	v_fma_f32 v109, v105, v137, v145
	v_fma_f32 v59, v95, v129, v66
	v_fma_f32 v109, v104, v136, v109
	v_fma_f32 v61, v94, v128, v59
	v_fma_f32 v135, v105, v135, v151
	v_fma_f32 v59, v63, v133, v67
	v_fma_f32 v135, v104, v134, v135
	v_and_b32_e32 v139, 0xffff0000, v227
	v_and_b32_e32 v138, 0xffff0000, v231
	v_fma_f32 v62, v62, v132, v59
	v_pk_mov_b32 v[140:141], v[138:139], v[140:141] op_sel:[1,0]
	v_fma_f32 v59, v97, v137, v68
	v_fma_f32 v63, v96, v136, v59
	v_cvt_pk_bf16_f32 v108, v142, v108
	v_fma_f32 v59, v65, v141, v69
	v_fma_f32 v64, v64, v140, v59
	v_lshlrev_b32_e32 v58, 16, v232
	v_mov_b32_e32 v59, v110
	v_fma_f32 v143, v77, v141, v146
	v_fma_f32 v59, v99, v59, v70
	v_fma_f32 v65, v98, v58, v59
	v_and_b32_e32 v58, 0xffff0000, v232
	v_mov_b32_e32 v59, v114
	v_fma_f32 v144, v76, v140, v143
	v_fma_f32 v59, v87, v59, v71
	v_fma_f32 v66, v86, v58, v59
	v_lshlrev_b32_e32 v58, 16, v233
	v_mov_b32_e32 v59, v118
	v_pk_mul_f32 v[142:143], v[76:77], v[138:139]
	v_fma_f32 v59, v101, v59, v72
	v_fma_f32 v67, v100, v58, v59
	v_and_b32_e32 v58, 0xffff0000, v233
	v_mov_b32_e32 v59, v122
	v_add_f32_e32 v139, v143, v152
	v_fma_f32 v59, v89, v59, v60
	v_fma_f32 v60, v88, v58, v59
	v_lshlrev_b32_e32 v58, 16, v234
	v_mov_b32_e32 v59, v126
	v_cvt_pk_bf16_f32 v109, v109, v144
	ds_write_b128 v147, v[106:109]
	v_fma_f32 v59, v103, v59, v61
	v_fma_f32 v61, v102, v58, v59
	v_and_b32_e32 v58, 0xffff0000, v234
	v_mov_b32_e32 v59, v130
	v_add_f32_e32 v109, v142, v139
	v_fma_f32 v59, v75, v59, v62
	v_fma_f32 v62, v74, v58, v59
	v_lshlrev_b32_e32 v58, 16, v235
	v_mov_b32_e32 v59, v134
	v_cvt_pk_bf16_f32 v106, v111, v115
	v_add3_u32 v111, s49, v188, v189
	v_fma_f32 v59, v105, v59, v63
	v_fma_f32 v63, v104, v58, v59
	v_and_b32_e32 v58, 0xffff0000, v235
	v_mov_b32_e32 v59, v138
	v_cvt_pk_bf16_f32 v107, v119, v123
	v_cvt_pk_bf16_f32 v108, v127, v131
	v_cvt_pk_bf16_f32 v109, v135, v109
	ds_write_b128 v111, v[106:109]
	v_fma_f32 v59, v77, v59, v64
	v_fma_f32 v64, v76, v58, v59
	v_cvt_pk_bf16_f32 v58, v65, v66
	v_cvt_pk_bf16_f32 v59, v67, v60
	v_cvt_pk_bf16_f32 v60, v61, v62
	v_add3_u32 v62, s49, v190, v191
	v_cvt_pk_bf16_f32 v61, v63, v64
	ds_write_b128 v62, v[58:61]
	v_add_u32_e32 v58, s53, v192
	v_add_u32_e32 v242, v58, v193
	s_waitcnt lgkmcnt(0)
	s_barrier
	ds_read_b128 v[58:61], v242
	ds_read_b128 v[62:65], v242 offset:4096
	ds_read_b128 v[98:101], v242 offset:8192
	ds_read_b128 v[102:105], v242 offset:12288
	s_waitcnt lgkmcnt(3)
	v_mfma_f32_16x16x32_bf16 v[66:69], v[42:45], v[58:61], 0
	v_mfma_f32_16x16x32_bf16 v[70:73], v[46:49], v[58:61], 0
	v_mfma_f32_16x16x32_bf16 v[74:77], v[50:53], v[58:61], 0
	s_waitcnt vmcnt(3)
	v_mfma_f32_16x16x32_bf16 v[58:61], v[54:57], v[58:61], 0
	s_waitcnt lgkmcnt(2)
	v_mfma_f32_16x16x32_bf16 v[86:89], v[42:45], v[62:65], 0
	v_mfma_f32_16x16x32_bf16 v[90:93], v[46:49], v[62:65], 0
	v_mfma_f32_16x16x32_bf16 v[94:97], v[50:53], v[62:65], 0
	v_mfma_f32_16x16x32_bf16 v[62:65], v[54:57], v[62:65], 0
	s_waitcnt lgkmcnt(1)
	v_mfma_f32_16x16x32_bf16 v[106:109], v[42:45], v[98:101], 0
	v_mfma_f32_16x16x32_bf16 v[110:113], v[46:49], v[98:101], 0
	v_mfma_f32_16x16x32_bf16 v[114:117], v[50:53], v[98:101], 0
	v_mfma_f32_16x16x32_bf16 v[98:101], v[54:57], v[98:101], 0
	s_waitcnt lgkmcnt(0)
	v_mfma_f32_16x16x32_bf16 v[42:45], v[42:45], v[102:105], 0
	v_mfma_f32_16x16x32_bf16 v[46:49], v[46:49], v[102:105], 0
	v_mfma_f32_16x16x32_bf16 v[50:53], v[50:53], v[102:105], 0
	v_mfma_f32_16x16x32_bf16 v[54:57], v[54:57], v[102:105], 0
	v_add_u32_e32 v102, s53, v194
	v_add_u32_e32 v243, v102, v193
	ds_read_b128 v[102:105], v243
	ds_read_b128 v[118:121], v243 offset:4096
	s_waitcnt lgkmcnt(1)
	v_mfma_f32_16x16x32_bf16 v[66:69], v[26:29], v[102:105], v[66:69]
	v_mfma_f32_16x16x32_bf16 v[70:73], v[30:33], v[102:105], v[70:73]
	v_mfma_f32_16x16x32_bf16 v[74:77], v[34:37], v[102:105], v[74:77]
	s_waitcnt vmcnt(2)
	v_mfma_f32_16x16x32_bf16 v[58:61], v[38:41], v[102:105], v[58:61]
	s_waitcnt lgkmcnt(0)
	v_mfma_f32_16x16x32_bf16 v[86:89], v[26:29], v[118:121], v[86:89]
	v_mfma_f32_16x16x32_bf16 v[90:93], v[30:33], v[118:121], v[90:93]
	v_mfma_f32_16x16x32_bf16 v[94:97], v[34:37], v[118:121], v[94:97]
	v_mfma_f32_16x16x32_bf16 v[62:65], v[38:41], v[118:121], v[62:65]
	ds_read_b128 v[102:105], v243 offset:8192
	ds_read_b128 v[118:121], v243 offset:12288
	s_waitcnt lgkmcnt(1)
	v_mfma_f32_16x16x32_bf16 v[106:109], v[26:29], v[102:105], v[106:109]
	s_waitcnt lgkmcnt(0)
	v_mfma_f32_16x16x32_bf16 v[26:29], v[26:29], v[118:121], v[42:45]
	s_nop 2
	v_add_u32_e32 v42, s53, v195
	v_add_u32_e32 v244, v42, v193
	v_mfma_f32_16x16x32_bf16 v[110:113], v[30:33], v[102:105], v[110:113]
	v_mfma_f32_16x16x32_bf16 v[30:33], v[30:33], v[118:121], v[46:49]
	ds_read_b128 v[42:45], v244
	s_nop 1
	ds_read_b128 v[46:49], v244 offset:4096
	v_mfma_f32_16x16x32_bf16 v[114:117], v[34:37], v[102:105], v[114:117]
	v_mfma_f32_16x16x32_bf16 v[98:101], v[38:41], v[102:105], v[98:101]
	v_mfma_f32_16x16x32_bf16 v[34:37], v[34:37], v[118:121], v[50:53]
	v_mfma_f32_16x16x32_bf16 v[38:41], v[38:41], v[118:121], v[54:57]
	s_waitcnt lgkmcnt(1)
	v_mfma_f32_16x16x32_bf16 v[50:53], v[10:13], v[42:45], v[66:69]
	v_mfma_f32_16x16x32_bf16 v[54:57], v[14:17], v[42:45], v[70:73]
	v_mfma_f32_16x16x32_bf16 v[66:69], v[18:21], v[42:45], v[74:77]
	s_waitcnt vmcnt(1)
	v_mfma_f32_16x16x32_bf16 v[42:45], v[22:25], v[42:45], v[58:61]
	s_waitcnt lgkmcnt(0)
	v_mfma_f32_16x16x32_bf16 v[58:61], v[10:13], v[46:49], v[86:89]
	v_mfma_f32_16x16x32_bf16 v[70:73], v[14:17], v[46:49], v[90:93]
	v_mfma_f32_16x16x32_bf16 v[74:77], v[18:21], v[46:49], v[94:97]
	v_mfma_f32_16x16x32_bf16 v[46:49], v[22:25], v[46:49], v[62:65]
	s_nop 2
	ds_read_b128 v[62:65], v244 offset:8192
	ds_read_b128 v[86:89], v244 offset:12288
	s_waitcnt lgkmcnt(1)
	v_mfma_f32_16x16x32_bf16 v[114:117], v[18:21], v[62:65], v[114:117]
	s_waitcnt lgkmcnt(0)
	v_mfma_f32_16x16x32_bf16 v[176:179], v[18:21], v[86:89], v[34:37]
	v_add_u32_e32 v18, s53, v196
	v_add_u32_e32 v241, v18, v193
	s_ashr_i32 s53, s52, 31
	v_mfma_f32_16x16x32_bf16 v[90:93], v[10:13], v[62:65], v[106:109]
	s_lshl_b64 s[52:53], s[52:53], 16
	v_mfma_f32_16x16x32_bf16 v[110:113], v[14:17], v[62:65], v[110:113]
	v_mfma_f32_16x16x32_bf16 v[62:65], v[22:25], v[62:65], v[98:101]
	v_mfma_f32_16x16x32_bf16 v[180:183], v[22:25], v[86:89], v[38:41]
	ds_read_b128 v[18:21], v241
	ds_read_b128 v[22:25], v241 offset:4096
	s_waitcnt lgkmcnt(1)
	v_mfma_f32_16x16x32_bf16 v[150:153], v[2:5], v[18:21], v[50:53]
	v_mfma_f32_16x16x32_bf16 v[146:149], v[6:9], v[18:21], v[54:57]
	v_mfma_f32_16x16x32_bf16 v[106:109], v[78:81], v[18:21], v[66:69]
	s_waitcnt vmcnt(0)
	v_mfma_f32_16x16x32_bf16 v[102:105], v[82:85], v[18:21], v[42:45]
	ds_read_b128 v[18:21], v241 offset:8192
	ds_read_b128 v[246:249], v241 offset:12288
	s_waitcnt lgkmcnt(2)
	v_mfma_f32_16x16x32_bf16 v[142:145], v[2:5], v[22:25], v[58:61]
	v_mfma_f32_16x16x32_bf16 v[138:141], v[6:9], v[22:25], v[70:73]
	v_mfma_f32_16x16x32_bf16 v[98:101], v[78:81], v[22:25], v[74:77]
	v_mfma_f32_16x16x32_bf16 v[94:97], v[82:85], v[22:25], v[46:49]
	v_add_u32_e32 v22, s48, v159
	v_ashrrev_i32_e32 v23, 31, v22
	v_lshlrev_b64 v[24:25], 2, v[22:23]
	v_lshl_add_u64 v[174:175], s[12:13], 0, v[24:25]
	s_waitcnt lgkmcnt(1)
	v_mfma_f32_16x16x32_bf16 v[134:137], v[2:5], v[18:21], v[90:93]
	v_lshl_add_u64 v[172:173], s[16:17], 0, v[24:25]
	v_add_u32_e32 v22, 16, v22
	v_ashrrev_i32_e32 v23, 31, v22
	v_mfma_f32_16x16x32_bf16 v[90:93], v[78:81], v[18:21], v[114:117]
	global_load_dwordx4 v[118:121], v[174:175], off
	global_load_dwordx4 v[74:77], v[174:175], off offset:64
	s_nop 0
	global_load_dwordx4 v[114:117], v[172:173], off
	global_load_dwordx4 v[70:73], v[172:173], off offset:64
	v_lshl_add_u64 v[168:169], s[18:19], 0, v[24:25]
	s_waitcnt vmcnt(3)
	v_pk_add_f32 v[150:151], v[118:119], v[150:151]
	v_mfma_f32_16x16x32_bf16 v[10:13], v[10:13], v[86:89], v[26:29]
	s_waitcnt vmcnt(1)
	v_pk_add_f32 v[146:147], v[114:115], v[146:147]
	v_pk_mul_f32 v[150:151], v[150:151], s[44:45] op_sel_hi:[1,0]
	v_pk_mul_f32 v[146:147], v[146:147], s[44:45] op_sel_hi:[1,0]
	v_mfma_f32_16x16x32_bf16 v[14:17], v[14:17], v[86:89], v[30:33]
	v_exp_f32_e32 v150, v150
	v_exp_f32_e32 v151, v151
	s_waitcnt lgkmcnt(0)
	v_mfma_f32_16x16x32_bf16 v[126:129], v[2:5], v[246:249], v[10:13]
	v_lshl_add_u64 v[2:3], v[22:23], 2, s[18:19]
	s_nop 1
	v_lshl_add_u64 v[10:11], v[156:157], 0, s[52:53]
	v_add_co_u32_e32 v12, vcc, s3, v10
	v_mfma_f32_16x16x32_bf16 v[130:133], v[6:9], v[18:21], v[110:113]
	s_nop 0
	v_addc_co_u32_e32 v13, vcc, 0, v11, vcc
	s_nop 0
	global_load_dwordx4 v[110:113], v[168:169], off
	global_load_dwordx4 v[66:69], v[2:3], off
	v_mfma_f32_16x16x32_bf16 v[122:125], v[6:9], v[246:249], v[14:17]
	v_add_co_u32_e32 v6, vcc, s29, v10
	s_nop 1
	v_addc_co_u32_e32 v7, vcc, 0, v11, vcc
	v_mfma_f32_16x16x32_bf16 v[86:89], v[82:85], v[18:21], v[62:65]
	global_load_dwordx4 v[46:49], v[10:11], off
	global_load_dwordx4 v[30:33], v[10:11], off offset:1024
	global_load_dwordx4 v[18:21], v[10:11], off offset:2048
	global_load_dwordx4 v[2:5], v[10:11], off offset:3072
	global_load_dwordx4 v[38:41], v[12:13], off offset:1024
	global_load_dwordx4 v[22:25], v[12:13], off offset:2048
	global_load_dwordx4 v[54:57], v[6:7], off offset:-4096
	global_load_dwordx4 v[58:61], v[6:7], off
	global_load_dwordx4 v[42:45], v[6:7], off offset:1024
	global_load_dwordx4 v[26:29], v[6:7], off offset:2048
	s_nop 0
	global_load_dwordx4 v[6:9], v[6:7], off offset:3072
	v_add_co_u32_e32 v10, vcc, s47, v10
	v_mfma_f32_16x16x32_bf16 v[78:81], v[78:81], v[246:249], v[176:179]
	s_nop 0
	v_addc_co_u32_e32 v11, vcc, 0, v11, vcc
	global_load_dwordx4 v[14:17], v[12:13], off offset:3072
	global_load_dwordx4 v[62:65], v[10:11], off
	global_load_dwordx4 v[50:53], v[10:11], off offset:1024
	global_load_dwordx4 v[34:37], v[10:11], off offset:2048
	s_nop 0
	global_load_dwordx4 v[10:13], v[10:11], off offset:3072
	v_exp_f32_e32 v176, v146
	v_exp_f32_e32 v177, v147
	v_pk_add_f32 v[146:147], v[150:151], 1.0 op_sel_hi:[1,0]
	v_mfma_f32_16x16x32_bf16 v[82:85], v[82:85], v[246:249], v[180:183]
	v_add_f32_e64 v176, v176, 1.0
	v_add_f32_e64 v177, v177, 1.0
	v_pk_mul_f32 v[150:151], v[146:147], v[176:177]
	s_nop 0
	v_rcp_f32_e32 v178, v150
	v_rcp_f32_e32 v179, v151
	v_add_u32_e32 v150, v245, v197
	v_add_u32_e32 v154, v150, v198
	ds_read_b64 v[150:151], v154
	v_pk_mul_f32 v[176:177], v[176:177], v[178:179]
	s_waitcnt vmcnt(17)
	v_pk_mul_f32 v[176:177], v[110:111], v[176:177]
	s_nop 0
	v_pk_mul_f32 v[182:183], v[176:177], s[98:99] op_sel_hi:[1,0]
	s_nop 0
	v_pk_fma_f32 v[180:181], v[182:183], s[46:47], v[164:165] op_sel_hi:[1,0,0]
	v_min_f32_e32 v170, v182, v183
	v_pk_fma_f32 v[180:181], v[182:183], v[180:181], 0.5 op_sel_hi:[1,1,0]
	v_cmp_ge_f32_e32 vcc, s66, v170
	v_pk_fma_f32 v[180:181], v[182:183], v[180:181], 1.0 op_sel_hi:[1,1,0]
	s_nop 0
	v_pk_mul_f32 v[180:181], v[180:181], v[182:183] neg_lo:[0,1] neg_hi:[0,1]
	s_and_b64 vcc, exec, vcc
	s_cbranch_vccnz .LBB0_1308
.LBB0_1263:
	v_pk_add_f32 v[152:153], v[120:121], v[152:153]
	v_pk_add_f32 v[148:149], v[116:117], v[148:149]
	v_pk_mul_f32 v[152:153], v[152:153], s[44:45] op_sel_hi:[1,0]
	v_pk_mul_f32 v[148:149], v[148:149], s[44:45] op_sel_hi:[1,0]
	v_exp_f32_e32 v152, v152
	v_exp_f32_e32 v153, v153
	v_exp_f32_e32 v148, v148
	v_exp_f32_e32 v149, v149
	v_pk_mul_f32 v[146:147], v[146:147], v[178:179]
	v_pk_add_f32 v[152:153], v[152:153], 1.0 op_sel_hi:[1,0]
	v_sqrt_f32_e32 v180, v180
	v_pk_add_f32 v[148:149], v[148:149], 1.0 op_sel_hi:[1,0]
	v_sqrt_f32_e32 v181, v181
	v_pk_mul_f32 v[178:179], v[152:153], v[148:149]
	s_waitcnt lgkmcnt(0)
	v_lshlrev_b32_e32 v182, 16, v150
	v_rcp_f32_e32 v178, v178
	v_rcp_f32_e32 v179, v179
	v_and_b32_e32 v183, 0xffff0000, v150
	v_pk_mul_f32 v[146:147], v[146:147], v[180:181]
	v_pk_mul_f32 v[148:149], v[148:149], v[178:179]
	s_nop 0
	v_pk_mul_f32 v[148:149], v[112:113], v[148:149]
	v_pk_mul_f32 v[146:147], v[146:147], v[182:183]
	v_pk_mul_f32 v[180:181], v[148:149], s[98:99] op_sel_hi:[1,0]
	v_cvt_pk_bf16_f32 v146, v176, v146
	v_cvt_pk_bf16_f32 v147, v177, v147
	s_nop 0
	v_pk_fma_f32 v[176:177], v[180:181], s[46:47], v[164:165] op_sel_hi:[1,0,0]
	v_min_f32_e32 v150, v180, v181
	v_pk_fma_f32 v[176:177], v[180:181], v[176:177], 0.5 op_sel_hi:[1,1,0]
	v_cmp_ge_f32_e32 vcc, s66, v150
	v_pk_fma_f32 v[176:177], v[180:181], v[176:177], 1.0 op_sel_hi:[1,1,0]
	s_nop 0
	v_pk_mul_f32 v[176:177], v[176:177], v[180:181] neg_lo:[0,1] neg_hi:[0,1]
	s_and_b64 vcc, exec, vcc
	s_cbranch_vccnz .LBB0_1309
.LBB0_1264:
	v_sqrt_f32_e32 v176, v176
	v_sqrt_f32_e32 v177, v177
	v_pk_add_f32 v[142:143], v[118:119], v[142:143]
	v_pk_add_f32 v[138:139], v[114:115], v[138:139]
	v_pk_mul_f32 v[152:153], v[152:153], v[178:179]
	v_pk_mul_f32 v[142:143], v[142:143], s[44:45] op_sel_hi:[1,0]
	v_pk_mul_f32 v[138:139], v[138:139], s[44:45] op_sel_hi:[1,0]
	v_pk_mul_f32 v[152:153], v[152:153], v[176:177]
	v_exp_f32_e32 v142, v142
	v_exp_f32_e32 v143, v143
	v_exp_f32_e32 v176, v138
	v_exp_f32_e32 v177, v139
	v_lshlrev_b32_e32 v150, 16, v151
	v_pk_add_f32 v[138:139], v[142:143], 1.0 op_sel_hi:[1,0]
	v_and_b32_e32 v151, 0xffff0000, v151
	v_pk_add_f32 v[176:177], v[176:177], 1.0 op_sel_hi:[1,0]
	v_pk_mul_f32 v[152:153], v[152:153], v[150:151]
	v_pk_mul_f32 v[142:143], v[138:139], v[176:177]
	v_cvt_pk_bf16_f32 v148, v148, v152
	v_cvt_pk_bf16_f32 v149, v149, v153
	ds_write_b128 v236, v[146:149]
	v_rcp_f32_e32 v150, v142
	v_rcp_f32_e32 v151, v143
	ds_read_b64 v[142:143], v154 offset:4096
	v_pk_mul_f32 v[146:147], v[176:177], v[150:151]
	s_nop 0
	v_pk_mul_f32 v[146:147], v[110:111], v[146:147]
	s_nop 0
	v_pk_mul_f32 v[152:153], v[146:147], s[98:99] op_sel_hi:[1,0]
	s_nop 0
	v_pk_fma_f32 v[148:149], v[152:153], s[46:47], v[164:165] op_sel_hi:[1,0,0]
	v_min_f32_e32 v170, v152, v153
	v_pk_fma_f32 v[148:149], v[152:153], v[148:149], 0.5 op_sel_hi:[1,1,0]
	v_cmp_ge_f32_e32 vcc, s66, v170
	v_pk_fma_f32 v[148:149], v[152:153], v[148:149], 1.0 op_sel_hi:[1,1,0]
	s_nop 0
	v_pk_mul_f32 v[148:149], v[148:149], v[152:153] neg_lo:[0,1] neg_hi:[0,1]
	s_and_b64 vcc, exec, vcc
	s_cbranch_vccnz .LBB0_1310
.LBB0_1265:
	v_pk_add_f32 v[144:145], v[120:121], v[144:145]
	v_pk_add_f32 v[140:141], v[116:117], v[140:141]
	v_pk_mul_f32 v[144:145], v[144:145], s[44:45] op_sel_hi:[1,0]
	v_pk_mul_f32 v[140:141], v[140:141], s[44:45] op_sel_hi:[1,0]
	v_exp_f32_e32 v144, v144
	v_exp_f32_e32 v145, v145
	v_exp_f32_e32 v140, v140
	v_exp_f32_e32 v141, v141
	v_sqrt_f32_e32 v148, v148
	v_sqrt_f32_e32 v149, v149
	v_pk_mul_f32 v[138:139], v[138:139], v[150:151]
	v_pk_add_f32 v[144:145], v[144:145], 1.0 op_sel_hi:[1,0]
	v_pk_add_f32 v[140:141], v[140:141], 1.0 op_sel_hi:[1,0]
	v_pk_mul_f32 v[138:139], v[138:139], v[148:149]
	v_pk_mul_f32 v[148:149], v[144:145], v[140:141]
	s_waitcnt lgkmcnt(0)
	v_lshlrev_b32_e32 v152, 16, v142
	v_rcp_f32_e32 v148, v148
	v_rcp_f32_e32 v149, v149
	v_and_b32_e32 v153, 0xffff0000, v142
	v_pk_mul_f32 v[138:139], v[138:139], v[152:153]
	v_pk_mul_f32 v[140:141], v[140:141], v[148:149]
	s_nop 0
	v_pk_mul_f32 v[140:141], v[112:113], v[140:141]
	v_cvt_pk_bf16_f32 v138, v146, v138
	v_cvt_pk_bf16_f32 v139, v147, v139
	s_nop 0
	v_pk_mul_f32 v[146:147], v[140:141], s[98:99] op_sel_hi:[1,0]
	s_nop 0
	v_pk_fma_f32 v[150:151], v[146:147], s[46:47], v[164:165] op_sel_hi:[1,0,0]
	v_min_f32_e32 v142, v146, v147
	v_pk_fma_f32 v[150:151], v[146:147], v[150:151], 0.5 op_sel_hi:[1,1,0]
	v_cmp_ge_f32_e32 vcc, s66, v142
	v_pk_fma_f32 v[150:151], v[146:147], v[150:151], 1.0 op_sel_hi:[1,1,0]
	s_nop 0
	v_pk_mul_f32 v[150:151], v[150:151], v[146:147] neg_lo:[0,1] neg_hi:[0,1]
	s_and_b64 vcc, exec, vcc
	s_cbranch_vccnz .LBB0_1311
.LBB0_1266:
	v_sqrt_f32_e32 v146, v150
	v_sqrt_f32_e32 v147, v151
	v_pk_add_f32 v[134:135], v[118:119], v[134:135]
	v_pk_add_f32 v[130:131], v[114:115], v[130:131]
	v_pk_mul_f32 v[144:145], v[144:145], v[148:149]
	v_pk_mul_f32 v[134:135], v[134:135], s[44:45] op_sel_hi:[1,0]
	v_pk_mul_f32 v[130:131], v[130:131], s[44:45] op_sel_hi:[1,0]
	v_pk_mul_f32 v[144:145], v[144:145], v[146:147]
	v_exp_f32_e32 v134, v134
	v_exp_f32_e32 v135, v135
	v_exp_f32_e32 v146, v130
	v_exp_f32_e32 v147, v131
	v_lshlrev_b32_e32 v142, 16, v143
	v_pk_add_f32 v[130:131], v[134:135], 1.0 op_sel_hi:[1,0]
	v_and_b32_e32 v143, 0xffff0000, v143
	v_pk_add_f32 v[146:147], v[146:147], 1.0 op_sel_hi:[1,0]
	v_pk_mul_f32 v[144:145], v[144:145], v[142:143]
	v_pk_mul_f32 v[134:135], v[130:131], v[146:147]
	v_cvt_pk_bf16_f32 v140, v140, v144
	v_cvt_pk_bf16_f32 v141, v141, v145
	ds_write_b128 v236, v[138:141] offset:2432
	v_rcp_f32_e32 v142, v134
	v_rcp_f32_e32 v143, v135
	ds_read_b64 v[134:135], v154 offset:8192
	v_pk_mul_f32 v[138:139], v[146:147], v[142:143]
	s_nop 0
	v_pk_mul_f32 v[138:139], v[110:111], v[138:139]
	s_nop 0
	v_pk_mul_f32 v[144:145], v[138:139], s[98:99] op_sel_hi:[1,0]
	s_nop 0
	v_pk_fma_f32 v[140:141], v[144:145], s[46:47], v[164:165] op_sel_hi:[1,0,0]
	v_min_f32_e32 v146, v144, v145
	v_pk_fma_f32 v[140:141], v[144:145], v[140:141], 0.5 op_sel_hi:[1,1,0]
	v_cmp_ge_f32_e32 vcc, s66, v146
	v_pk_fma_f32 v[140:141], v[144:145], v[140:141], 1.0 op_sel_hi:[1,1,0]
	s_nop 0
	v_pk_mul_f32 v[140:141], v[140:141], v[144:145] neg_lo:[0,1] neg_hi:[0,1]
	s_and_b64 vcc, exec, vcc
	s_cbranch_vccnz .LBB0_1312
.LBB0_1267:
	v_pk_add_f32 v[136:137], v[120:121], v[136:137]
	v_pk_add_f32 v[132:133], v[116:117], v[132:133]
	v_pk_mul_f32 v[136:137], v[136:137], s[44:45] op_sel_hi:[1,0]
	v_pk_mul_f32 v[132:133], v[132:133], s[44:45] op_sel_hi:[1,0]
	v_exp_f32_e32 v136, v136
	v_exp_f32_e32 v137, v137
	v_exp_f32_e32 v132, v132
	v_exp_f32_e32 v133, v133
	v_sqrt_f32_e32 v140, v140
	v_sqrt_f32_e32 v141, v141
	v_pk_mul_f32 v[130:131], v[130:131], v[142:143]
	v_pk_add_f32 v[136:137], v[136:137], 1.0 op_sel_hi:[1,0]
	v_pk_add_f32 v[132:133], v[132:133], 1.0 op_sel_hi:[1,0]
	v_pk_mul_f32 v[130:131], v[130:131], v[140:141]
	v_pk_mul_f32 v[140:141], v[136:137], v[132:133]
	s_waitcnt lgkmcnt(0)
	v_lshlrev_b32_e32 v144, 16, v134
	v_rcp_f32_e32 v140, v140
	v_rcp_f32_e32 v141, v141
	v_and_b32_e32 v145, 0xffff0000, v134
	v_pk_mul_f32 v[130:131], v[130:131], v[144:145]
	v_pk_mul_f32 v[132:133], v[132:133], v[140:141]
	s_nop 0
	v_pk_mul_f32 v[132:133], v[112:113], v[132:133]
	v_cvt_pk_bf16_f32 v130, v138, v130
	v_cvt_pk_bf16_f32 v131, v139, v131
	s_nop 0
	v_pk_mul_f32 v[138:139], v[132:133], s[98:99] op_sel_hi:[1,0]
	s_nop 0
	v_pk_fma_f32 v[142:143], v[138:139], s[46:47], v[164:165] op_sel_hi:[1,0,0]
	v_min_f32_e32 v134, v138, v139
	v_pk_fma_f32 v[142:143], v[138:139], v[142:143], 0.5 op_sel_hi:[1,1,0]
	v_cmp_ge_f32_e32 vcc, s66, v134
	v_pk_fma_f32 v[142:143], v[138:139], v[142:143], 1.0 op_sel_hi:[1,1,0]
	s_nop 0
	v_pk_mul_f32 v[142:143], v[142:143], v[138:139] neg_lo:[0,1] neg_hi:[0,1]
	s_and_b64 vcc, exec, vcc
	s_cbranch_vccnz .LBB0_1313
.LBB0_1268:
	v_pk_add_f32 v[118:119], v[118:119], v[126:127]
	v_pk_add_f32 v[114:115], v[114:115], v[122:123]
	v_sqrt_f32_e32 v138, v142
	v_sqrt_f32_e32 v139, v143
	v_pk_mul_f32 v[118:119], v[118:119], s[44:45] op_sel_hi:[1,0]
	v_pk_mul_f32 v[114:115], v[114:115], s[44:45] op_sel_hi:[1,0]
	v_exp_f32_e32 v118, v118
	v_exp_f32_e32 v119, v119
	v_exp_f32_e32 v114, v114
	v_exp_f32_e32 v115, v115
	v_pk_mul_f32 v[136:137], v[136:137], v[140:141]
	v_lshlrev_b32_e32 v134, 16, v135
	v_and_b32_e32 v135, 0xffff0000, v135
	v_pk_mul_f32 v[136:137], v[136:137], v[138:139]
	v_pk_add_f32 v[118:119], v[118:119], 1.0 op_sel_hi:[1,0]
	v_pk_mul_f32 v[126:127], v[136:137], v[134:135]
	v_pk_add_f32 v[134:135], v[114:115], 1.0 op_sel_hi:[1,0]
	v_cvt_pk_bf16_f32 v132, v132, v126
	v_cvt_pk_bf16_f32 v133, v133, v127
	ds_write_b128 v236, v[130:133] offset:4864
	v_pk_mul_f32 v[114:115], v[118:119], v[134:135]
	s_nop 0
	v_rcp_f32_e32 v122, v114
	v_rcp_f32_e32 v123, v115
	ds_read_b64 v[114:115], v154 offset:12288
	v_pk_mul_f32 v[126:127], v[134:135], v[122:123]
	s_nop 0
	v_pk_mul_f32 v[110:111], v[110:111], v[126:127]
	s_nop 0
	v_pk_mul_f32 v[130:131], v[110:111], s[98:99] op_sel_hi:[1,0]
	s_nop 0
	v_pk_fma_f32 v[126:127], v[130:131], s[46:47], v[164:165] op_sel_hi:[1,0,0]
	v_min_f32_e32 v132, v130, v131
	v_pk_fma_f32 v[126:127], v[130:131], v[126:127], 0.5 op_sel_hi:[1,1,0]
	v_cmp_ge_f32_e32 vcc, s66, v132
	v_pk_fma_f32 v[126:127], v[130:131], v[126:127], 1.0 op_sel_hi:[1,1,0]
	s_nop 0
	v_pk_mul_f32 v[126:127], v[126:127], v[130:131] neg_lo:[0,1] neg_hi:[0,1]
	s_and_b64 vcc, exec, vcc
	s_cbranch_vccnz .LBB0_1314
.LBB0_1269:
	v_pk_add_f32 v[120:121], v[120:121], v[128:129]
	v_pk_add_f32 v[116:117], v[116:117], v[124:125]
	v_pk_mul_f32 v[120:121], v[120:121], s[44:45] op_sel_hi:[1,0]
	v_pk_mul_f32 v[116:117], v[116:117], s[44:45] op_sel_hi:[1,0]
	v_sqrt_f32_e32 v126, v126
	v_sqrt_f32_e32 v127, v127
	v_exp_f32_e32 v120, v120
	v_exp_f32_e32 v121, v121
	v_exp_f32_e32 v128, v116
	v_exp_f32_e32 v129, v117
	v_pk_mul_f32 v[116:117], v[118:119], v[122:123]
	s_waitcnt lgkmcnt(0)
	v_lshlrev_b32_e32 v124, 16, v114
	v_pk_mul_f32 v[122:123], v[116:117], v[126:127]
	v_pk_add_f32 v[116:117], v[120:121], 1.0 op_sel_hi:[1,0]
	v_pk_add_f32 v[120:121], v[128:129], 1.0 op_sel_hi:[1,0]
	v_and_b32_e32 v125, 0xffff0000, v114
	v_pk_mul_f32 v[118:119], v[116:117], v[120:121]
	v_pk_mul_f32 v[122:123], v[122:123], v[124:125]
	v_rcp_f32_e32 v118, v118
	v_rcp_f32_e32 v119, v119
	v_cvt_pk_bf16_f32 v110, v110, v122
	v_cvt_pk_bf16_f32 v111, v111, v123
	s_nop 0
	v_pk_mul_f32 v[120:121], v[120:121], v[118:119]
	s_nop 0
	v_pk_mul_f32 v[112:113], v[112:113], v[120:121]
	s_nop 0
	v_pk_mul_f32 v[120:121], v[112:113], s[98:99] op_sel_hi:[1,0]
	s_nop 0
	v_pk_fma_f32 v[122:123], v[120:121], s[46:47], v[164:165] op_sel_hi:[1,0,0]
	v_min_f32_e32 v114, v120, v121
	v_pk_fma_f32 v[122:123], v[120:121], v[122:123], 0.5 op_sel_hi:[1,1,0]
	v_cmp_ge_f32_e32 vcc, s66, v114
	v_pk_fma_f32 v[122:123], v[120:121], v[122:123], 1.0 op_sel_hi:[1,1,0]
	s_nop 0
	v_pk_mul_f32 v[122:123], v[122:123], v[120:121] neg_lo:[0,1] neg_hi:[0,1]
	s_and_b64 vcc, exec, vcc
	s_cbranch_vccnz .LBB0_1315
.LBB0_1270:
	v_sqrt_f32_e32 v120, v122
	v_sqrt_f32_e32 v121, v123
	v_pk_mul_f32 v[116:117], v[116:117], v[118:119]
	v_pk_add_f32 v[106:107], v[74:75], v[106:107]
	v_pk_add_f32 v[102:103], v[70:71], v[102:103]
	v_lshlrev_b32_e32 v114, 16, v115
	v_and_b32_e32 v115, 0xffff0000, v115
	v_pk_mul_f32 v[116:117], v[116:117], v[120:121]
	v_pk_mul_f32 v[106:107], v[106:107], s[44:45] op_sel_hi:[1,0]
	v_pk_mul_f32 v[102:103], v[102:103], s[44:45] op_sel_hi:[1,0]
	v_pk_mul_f32 v[114:115], v[116:117], v[114:115]
	v_exp_f32_e32 v106, v106
	v_exp_f32_e32 v107, v107
	v_exp_f32_e32 v116, v102
	v_exp_f32_e32 v117, v103
	v_cvt_pk_bf16_f32 v112, v112, v114
	v_cvt_pk_bf16_f32 v113, v113, v115
	ds_write_b128 v236, v[110:113] offset:7296
	v_pk_add_f32 v[102:103], v[106:107], 1.0 op_sel_hi:[1,0]
	v_pk_add_f32 v[110:111], v[116:117], 1.0 op_sel_hi:[1,0]
	s_nop 0
	v_pk_mul_f32 v[106:107], v[102:103], v[110:111]
	s_nop 0
	v_rcp_f32_e32 v112, v106
	v_rcp_f32_e32 v113, v107
	v_add_u32_e32 v106, v245, v199
	v_add_u32_e32 v118, v106, v198
	ds_read_b64 v[106:107], v118
	v_pk_mul_f32 v[110:111], v[110:111], v[112:113]
	s_waitcnt vmcnt(16)
	v_pk_mul_f32 v[110:111], v[66:67], v[110:111]
	s_nop 0
	v_pk_mul_f32 v[116:117], v[110:111], s[98:99] op_sel_hi:[1,0]
	s_nop 0
	v_pk_fma_f32 v[114:115], v[116:117], s[46:47], v[164:165] op_sel_hi:[1,0,0]
	v_min_f32_e32 v119, v116, v117
	v_pk_fma_f32 v[114:115], v[116:117], v[114:115], 0.5 op_sel_hi:[1,1,0]
	v_cmp_ge_f32_e32 vcc, s66, v119
	v_pk_fma_f32 v[114:115], v[116:117], v[114:115], 1.0 op_sel_hi:[1,1,0]
	s_nop 0
	v_pk_mul_f32 v[114:115], v[114:115], v[116:117] neg_lo:[0,1] neg_hi:[0,1]
	s_and_b64 vcc, exec, vcc
	s_cbranch_vccnz .LBB0_1316
.LBB0_1271:
	v_pk_add_f32 v[108:109], v[76:77], v[108:109]
	v_pk_add_f32 v[104:105], v[72:73], v[104:105]
	v_pk_mul_f32 v[108:109], v[108:109], s[44:45] op_sel_hi:[1,0]
	v_pk_mul_f32 v[104:105], v[104:105], s[44:45] op_sel_hi:[1,0]
	v_exp_f32_e32 v108, v108
	v_exp_f32_e32 v109, v109
	v_exp_f32_e32 v104, v104
	v_exp_f32_e32 v105, v105
	v_pk_mul_f32 v[102:103], v[102:103], v[112:113]
	v_pk_add_f32 v[108:109], v[108:109], 1.0 op_sel_hi:[1,0]
	v_sqrt_f32_e32 v114, v114
	v_pk_add_f32 v[104:105], v[104:105], 1.0 op_sel_hi:[1,0]
	v_sqrt_f32_e32 v115, v115
	v_pk_mul_f32 v[112:113], v[108:109], v[104:105]
	s_waitcnt lgkmcnt(0)
	v_lshlrev_b32_e32 v116, 16, v106
	v_rcp_f32_e32 v112, v112
	v_rcp_f32_e32 v113, v113
	v_and_b32_e32 v117, 0xffff0000, v106
	v_pk_mul_f32 v[102:103], v[102:103], v[114:115]
	v_pk_mul_f32 v[104:105], v[104:105], v[112:113]
	s_nop 0
	v_pk_mul_f32 v[104:105], v[68:69], v[104:105]
	v_pk_mul_f32 v[102:103], v[102:103], v[116:117]
	v_pk_mul_f32 v[114:115], v[104:105], s[98:99] op_sel_hi:[1,0]
	v_cvt_pk_bf16_f32 v102, v110, v102
	v_cvt_pk_bf16_f32 v103, v111, v103
	s_nop 0
	v_pk_fma_f32 v[110:111], v[114:115], s[46:47], v[164:165] op_sel_hi:[1,0,0]
	v_min_f32_e32 v106, v114, v115
	v_pk_fma_f32 v[110:111], v[114:115], v[110:111], 0.5 op_sel_hi:[1,1,0]
	v_cmp_ge_f32_e32 vcc, s66, v106
	v_pk_fma_f32 v[110:111], v[114:115], v[110:111], 1.0 op_sel_hi:[1,1,0]
	s_nop 0
	v_pk_mul_f32 v[110:111], v[110:111], v[114:115] neg_lo:[0,1] neg_hi:[0,1]
	s_and_b64 vcc, exec, vcc
	s_cbranch_vccnz .LBB0_1317
.LBB0_1272:
	v_sqrt_f32_e32 v110, v110
	v_sqrt_f32_e32 v111, v111
	v_pk_add_f32 v[98:99], v[74:75], v[98:99]
	v_pk_add_f32 v[94:95], v[70:71], v[94:95]
	v_pk_mul_f32 v[108:109], v[108:109], v[112:113]
	v_pk_mul_f32 v[98:99], v[98:99], s[44:45] op_sel_hi:[1,0]
	v_pk_mul_f32 v[94:95], v[94:95], s[44:45] op_sel_hi:[1,0]
	v_pk_mul_f32 v[108:109], v[108:109], v[110:111]
	v_exp_f32_e32 v98, v98
	v_exp_f32_e32 v99, v99
	v_exp_f32_e32 v110, v94
	v_exp_f32_e32 v111, v95
	v_lshlrev_b32_e32 v106, 16, v107
	v_pk_add_f32 v[94:95], v[98:99], 1.0 op_sel_hi:[1,0]
	v_and_b32_e32 v107, 0xffff0000, v107
	v_pk_add_f32 v[110:111], v[110:111], 1.0 op_sel_hi:[1,0]
	v_pk_mul_f32 v[108:109], v[108:109], v[106:107]
	v_pk_mul_f32 v[98:99], v[94:95], v[110:111]
	v_cvt_pk_bf16_f32 v104, v104, v108
	v_cvt_pk_bf16_f32 v105, v105, v109
	ds_write_b128 v236, v[102:105] offset:64
	v_rcp_f32_e32 v106, v98
	v_rcp_f32_e32 v107, v99
	ds_read_b64 v[98:99], v118 offset:4096
	v_pk_mul_f32 v[102:103], v[110:111], v[106:107]
	s_nop 0
	v_pk_mul_f32 v[102:103], v[66:67], v[102:103]
	s_nop 0
	v_pk_mul_f32 v[108:109], v[102:103], s[98:99] op_sel_hi:[1,0]
	s_nop 0
	v_pk_fma_f32 v[104:105], v[108:109], s[46:47], v[164:165] op_sel_hi:[1,0,0]
	v_min_f32_e32 v110, v108, v109
	v_pk_fma_f32 v[104:105], v[108:109], v[104:105], 0.5 op_sel_hi:[1,1,0]
	v_cmp_ge_f32_e32 vcc, s66, v110
	v_pk_fma_f32 v[104:105], v[108:109], v[104:105], 1.0 op_sel_hi:[1,1,0]
	s_nop 0
	v_pk_mul_f32 v[104:105], v[104:105], v[108:109] neg_lo:[0,1] neg_hi:[0,1]
	s_and_b64 vcc, exec, vcc
	s_cbranch_vccnz .LBB0_1318
.LBB0_1273:
	v_pk_add_f32 v[100:101], v[76:77], v[100:101]
	v_pk_add_f32 v[96:97], v[72:73], v[96:97]
	v_pk_mul_f32 v[100:101], v[100:101], s[44:45] op_sel_hi:[1,0]
	v_pk_mul_f32 v[96:97], v[96:97], s[44:45] op_sel_hi:[1,0]
	v_exp_f32_e32 v100, v100
	v_exp_f32_e32 v101, v101
	v_exp_f32_e32 v96, v96
	v_exp_f32_e32 v97, v97
	v_sqrt_f32_e32 v104, v104
	v_sqrt_f32_e32 v105, v105
	v_pk_mul_f32 v[94:95], v[94:95], v[106:107]
	v_pk_add_f32 v[100:101], v[100:101], 1.0 op_sel_hi:[1,0]
	v_pk_add_f32 v[96:97], v[96:97], 1.0 op_sel_hi:[1,0]
	v_pk_mul_f32 v[94:95], v[94:95], v[104:105]
	v_pk_mul_f32 v[104:105], v[100:101], v[96:97]
	s_waitcnt lgkmcnt(0)
	v_lshlrev_b32_e32 v108, 16, v98
	v_rcp_f32_e32 v104, v104
	v_rcp_f32_e32 v105, v105
	v_and_b32_e32 v109, 0xffff0000, v98
	v_pk_mul_f32 v[94:95], v[94:95], v[108:109]
	v_pk_mul_f32 v[96:97], v[96:97], v[104:105]
	s_nop 0
	v_pk_mul_f32 v[96:97], v[68:69], v[96:97]
	v_cvt_pk_bf16_f32 v94, v102, v94
	v_cvt_pk_bf16_f32 v95, v103, v95
	s_nop 0
	v_pk_mul_f32 v[102:103], v[96:97], s[98:99] op_sel_hi:[1,0]
	s_nop 0
	v_pk_fma_f32 v[106:107], v[102:103], s[46:47], v[164:165] op_sel_hi:[1,0,0]
	v_min_f32_e32 v98, v102, v103
	v_pk_fma_f32 v[106:107], v[102:103], v[106:107], 0.5 op_sel_hi:[1,1,0]
	v_cmp_ge_f32_e32 vcc, s66, v98
	v_pk_fma_f32 v[106:107], v[102:103], v[106:107], 1.0 op_sel_hi:[1,1,0]
	s_nop 0
	v_pk_mul_f32 v[106:107], v[106:107], v[102:103] neg_lo:[0,1] neg_hi:[0,1]
	s_and_b64 vcc, exec, vcc
	s_cbranch_vccnz .LBB0_1319
.LBB0_1274:
	v_sqrt_f32_e32 v102, v106
	v_sqrt_f32_e32 v103, v107
	v_pk_add_f32 v[90:91], v[74:75], v[90:91]
	v_pk_add_f32 v[86:87], v[70:71], v[86:87]
	v_pk_mul_f32 v[100:101], v[100:101], v[104:105]
	v_pk_mul_f32 v[90:91], v[90:91], s[44:45] op_sel_hi:[1,0]
	v_pk_mul_f32 v[86:87], v[86:87], s[44:45] op_sel_hi:[1,0]
	v_pk_mul_f32 v[100:101], v[100:101], v[102:103]
	v_exp_f32_e32 v90, v90
	v_exp_f32_e32 v91, v91
	v_exp_f32_e32 v102, v86
	v_exp_f32_e32 v103, v87
	v_lshlrev_b32_e32 v98, 16, v99
	v_pk_add_f32 v[86:87], v[90:91], 1.0 op_sel_hi:[1,0]
	v_and_b32_e32 v99, 0xffff0000, v99
	v_pk_add_f32 v[102:103], v[102:103], 1.0 op_sel_hi:[1,0]
	v_pk_mul_f32 v[100:101], v[100:101], v[98:99]
	v_pk_mul_f32 v[90:91], v[86:87], v[102:103]
	v_cvt_pk_bf16_f32 v96, v96, v100
	v_cvt_pk_bf16_f32 v97, v97, v101
	ds_write_b128 v236, v[94:97] offset:2496
	v_rcp_f32_e32 v98, v90
	v_rcp_f32_e32 v99, v91
	ds_read_b64 v[90:91], v118 offset:8192
	v_pk_mul_f32 v[94:95], v[102:103], v[98:99]
	s_nop 0
	v_pk_mul_f32 v[94:95], v[66:67], v[94:95]
	s_nop 0
	v_pk_mul_f32 v[100:101], v[94:95], s[98:99] op_sel_hi:[1,0]
	s_nop 0
	v_pk_fma_f32 v[96:97], v[100:101], s[46:47], v[164:165] op_sel_hi:[1,0,0]
	v_min_f32_e32 v102, v100, v101
	v_pk_fma_f32 v[96:97], v[100:101], v[96:97], 0.5 op_sel_hi:[1,1,0]
	v_cmp_ge_f32_e32 vcc, s66, v102
	v_pk_fma_f32 v[96:97], v[100:101], v[96:97], 1.0 op_sel_hi:[1,1,0]
	s_nop 0
	v_pk_mul_f32 v[96:97], v[96:97], v[100:101] neg_lo:[0,1] neg_hi:[0,1]
	s_and_b64 vcc, exec, vcc
	s_cbranch_vccnz .LBB0_1320
.LBB0_1275:
	v_pk_add_f32 v[92:93], v[76:77], v[92:93]
	v_pk_add_f32 v[88:89], v[72:73], v[88:89]
	v_pk_mul_f32 v[92:93], v[92:93], s[44:45] op_sel_hi:[1,0]
	v_pk_mul_f32 v[88:89], v[88:89], s[44:45] op_sel_hi:[1,0]
	v_exp_f32_e32 v92, v92
	v_exp_f32_e32 v93, v93
	v_exp_f32_e32 v88, v88
	v_exp_f32_e32 v89, v89
	v_sqrt_f32_e32 v96, v96
	v_sqrt_f32_e32 v97, v97
	v_pk_mul_f32 v[86:87], v[86:87], v[98:99]
	v_pk_add_f32 v[92:93], v[92:93], 1.0 op_sel_hi:[1,0]
	v_pk_add_f32 v[88:89], v[88:89], 1.0 op_sel_hi:[1,0]
	v_pk_mul_f32 v[86:87], v[86:87], v[96:97]
	v_pk_mul_f32 v[96:97], v[92:93], v[88:89]
	s_waitcnt lgkmcnt(0)
	v_lshlrev_b32_e32 v100, 16, v90
	v_rcp_f32_e32 v96, v96
	v_rcp_f32_e32 v97, v97
	v_and_b32_e32 v101, 0xffff0000, v90
	v_pk_mul_f32 v[86:87], v[86:87], v[100:101]
	v_pk_mul_f32 v[88:89], v[88:89], v[96:97]
	s_nop 0
	v_pk_mul_f32 v[88:89], v[68:69], v[88:89]
	v_cvt_pk_bf16_f32 v86, v94, v86
	v_cvt_pk_bf16_f32 v87, v95, v87
	s_nop 0
	v_pk_mul_f32 v[94:95], v[88:89], s[98:99] op_sel_hi:[1,0]
	s_nop 0
	v_pk_fma_f32 v[98:99], v[94:95], s[46:47], v[164:165] op_sel_hi:[1,0,0]
	v_min_f32_e32 v90, v94, v95
	v_pk_fma_f32 v[98:99], v[94:95], v[98:99], 0.5 op_sel_hi:[1,1,0]
	v_cmp_ge_f32_e32 vcc, s66, v90
	v_pk_fma_f32 v[98:99], v[94:95], v[98:99], 1.0 op_sel_hi:[1,1,0]
	s_nop 0
	v_pk_mul_f32 v[98:99], v[98:99], v[94:95] neg_lo:[0,1] neg_hi:[0,1]
	s_and_b64 vcc, exec, vcc
	s_cbranch_vccnz .LBB0_1321
.LBB0_1276:
	v_pk_add_f32 v[74:75], v[74:75], v[78:79]
	v_pk_add_f32 v[70:71], v[70:71], v[82:83]
	v_sqrt_f32_e32 v94, v98
	v_sqrt_f32_e32 v95, v99
	v_pk_mul_f32 v[74:75], v[74:75], s[44:45] op_sel_hi:[1,0]
	v_pk_mul_f32 v[70:71], v[70:71], s[44:45] op_sel_hi:[1,0]
	v_exp_f32_e32 v74, v74
	v_exp_f32_e32 v75, v75
	v_exp_f32_e32 v70, v70
	v_exp_f32_e32 v71, v71
	v_pk_mul_f32 v[92:93], v[92:93], v[96:97]
	v_lshlrev_b32_e32 v90, 16, v91
	v_and_b32_e32 v91, 0xffff0000, v91
	v_pk_mul_f32 v[92:93], v[92:93], v[94:95]
	v_pk_add_f32 v[74:75], v[74:75], 1.0 op_sel_hi:[1,0]
	v_pk_mul_f32 v[82:83], v[92:93], v[90:91]
	v_pk_add_f32 v[90:91], v[70:71], 1.0 op_sel_hi:[1,0]
	v_cvt_pk_bf16_f32 v88, v88, v82
	v_cvt_pk_bf16_f32 v89, v89, v83
	ds_write_b128 v236, v[86:89] offset:4928
	v_pk_mul_f32 v[70:71], v[74:75], v[90:91]
	s_nop 0
	v_rcp_f32_e32 v78, v70
	v_rcp_f32_e32 v79, v71
	ds_read_b64 v[70:71], v118 offset:12288
	v_pk_mul_f32 v[82:83], v[90:91], v[78:79]
	s_nop 0
	v_pk_mul_f32 v[66:67], v[66:67], v[82:83]
	s_nop 0
	v_pk_mul_f32 v[86:87], v[66:67], s[98:99] op_sel_hi:[1,0]
	s_nop 0
	v_pk_fma_f32 v[82:83], v[86:87], s[46:47], v[164:165] op_sel_hi:[1,0,0]
	v_min_f32_e32 v88, v86, v87
	v_pk_fma_f32 v[82:83], v[86:87], v[82:83], 0.5 op_sel_hi:[1,1,0]
	v_cmp_ge_f32_e32 vcc, s66, v88
	v_pk_fma_f32 v[82:83], v[86:87], v[82:83], 1.0 op_sel_hi:[1,1,0]
	s_nop 0
	v_pk_mul_f32 v[82:83], v[82:83], v[86:87] neg_lo:[0,1] neg_hi:[0,1]
	s_and_b64 vcc, exec, vcc
	s_cbranch_vccnz .LBB0_1322
.LBB0_1277:
	v_pk_add_f32 v[76:77], v[76:77], v[80:81]
	v_pk_add_f32 v[72:73], v[72:73], v[84:85]
	v_pk_mul_f32 v[76:77], v[76:77], s[44:45] op_sel_hi:[1,0]
	v_pk_mul_f32 v[72:73], v[72:73], s[44:45] op_sel_hi:[1,0]
	v_sqrt_f32_e32 v82, v82
	v_sqrt_f32_e32 v83, v83
	v_exp_f32_e32 v76, v76
	v_exp_f32_e32 v77, v77
	v_exp_f32_e32 v84, v72
	v_exp_f32_e32 v85, v73
	v_pk_mul_f32 v[72:73], v[74:75], v[78:79]
	s_waitcnt lgkmcnt(0)
	v_lshlrev_b32_e32 v80, 16, v70
	v_pk_mul_f32 v[78:79], v[72:73], v[82:83]
	v_pk_add_f32 v[72:73], v[76:77], 1.0 op_sel_hi:[1,0]
	v_pk_add_f32 v[76:77], v[84:85], 1.0 op_sel_hi:[1,0]
	v_and_b32_e32 v81, 0xffff0000, v70
	v_pk_mul_f32 v[74:75], v[72:73], v[76:77]
	v_pk_mul_f32 v[78:79], v[78:79], v[80:81]
	v_rcp_f32_e32 v74, v74
	v_rcp_f32_e32 v75, v75
	v_cvt_pk_bf16_f32 v66, v66, v78
	v_cvt_pk_bf16_f32 v67, v67, v79
	s_nop 0
	v_pk_mul_f32 v[76:77], v[76:77], v[74:75]
	s_nop 0
	v_pk_mul_f32 v[68:69], v[68:69], v[76:77]
	s_nop 0
	v_pk_mul_f32 v[78:79], v[68:69], s[98:99] op_sel_hi:[1,0]
	s_nop 0
	v_pk_fma_f32 v[76:77], v[78:79], s[46:47], v[164:165] op_sel_hi:[1,0,0]
	v_min_f32_e32 v70, v78, v79
	v_pk_fma_f32 v[76:77], v[78:79], v[76:77], 0.5 op_sel_hi:[1,1,0]
	v_cmp_ge_f32_e32 vcc, s66, v70
	v_pk_fma_f32 v[76:77], v[78:79], v[76:77], 1.0 op_sel_hi:[1,1,0]
	s_nop 0
	v_pk_mul_f32 v[76:77], v[76:77], v[78:79] neg_lo:[0,1] neg_hi:[0,1]
	s_and_b64 vcc, exec, vcc
	s_cbranch_vccnz .LBB0_1323
.LBB0_1278:
	v_sqrt_f32_e32 v76, v76
	v_sqrt_f32_e32 v77, v77
	v_pk_mul_f32 v[72:73], v[72:73], v[74:75]
	v_lshlrev_b32_e32 v70, 16, v71
	v_and_b32_e32 v71, 0xffff0000, v71
	v_pk_mul_f32 v[72:73], v[72:73], v[76:77]
	s_lshl_b32 s81, s20, 1
	v_pk_mul_f32 v[70:71], v[72:73], v[70:71]
	s_ashr_i32 s49, s48, 31
	v_cvt_pk_bf16_f32 v68, v68, v70
	v_cvt_pk_bf16_f32 v69, v69, v71
	ds_write_b128 v236, v[66:69] offset:7360
	ds_read2_b64 v[66:69], v237 offset1:18
	s_add_i32 s81, s81, s30
	v_lshl_add_u64 v[94:95], s[48:49], 0, v[160:161]
	s_waitcnt lgkmcnt(0)
	v_lshlrev_b32_e32 v70, 16, v66
	v_lshlrev_b32_e32 v71, 16, v67
	v_add_f32_e32 v72, 0, v70
	v_add_f32_e32 v73, 0, v71
	v_exp_f32_e32 v70, v70
	v_exp_f32_e32 v71, v71
	v_and_b32_e32 v66, 0xffff0000, v66
	v_fmac_f32_e32 v66, 0, v70
	v_and_b32_e32 v67, 0xffff0000, v67
	v_lshlrev_b32_e32 v70, 16, v68
	v_fmac_f32_e32 v67, 0, v71
	v_lshlrev_b32_e32 v71, 16, v69
	v_add_f32_e32 v74, v72, v70
	v_exp_f32_e32 v76, v70
	v_add_f32_e32 v75, v73, v71
	v_exp_f32_e32 v77, v71
	ds_read2_b64 v[70:73], v237 offset0:36 offset1:54
	v_and_b32_e32 v68, 0xffff0000, v68
	v_fmac_f32_e32 v68, v76, v66
	v_and_b32_e32 v66, 0xffff0000, v69
	v_fmac_f32_e32 v66, v77, v67
	s_waitcnt lgkmcnt(0)
	v_lshlrev_b32_e32 v69, 16, v71
	v_lshlrev_b32_e32 v67, 16, v70
	v_add_f32_e32 v75, v75, v69
	v_add_f32_e32 v74, v74, v67
	v_exp_f32_e32 v69, v69
	v_exp_f32_e32 v67, v67
	v_and_b32_e32 v71, 0xffff0000, v71
	v_and_b32_e32 v70, 0xffff0000, v70
	v_fmac_f32_e32 v71, v69, v66
	v_lshlrev_b32_e32 v66, 16, v72
	v_fmac_f32_e32 v70, v67, v68
	v_lshlrev_b32_e32 v67, 16, v73
	v_add_f32_e32 v74, v74, v66
	v_exp_f32_e32 v76, v66
	v_add_f32_e32 v75, v75, v67
	v_exp_f32_e32 v77, v67
	ds_read2_b64 v[66:69], v237 offset0:72 offset1:90
	v_and_b32_e32 v72, 0xffff0000, v72
	v_fmac_f32_e32 v72, v76, v70
	v_and_b32_e32 v70, 0xffff0000, v73
	v_fmac_f32_e32 v70, v77, v71
	s_waitcnt lgkmcnt(0)
	v_lshlrev_b32_e32 v73, 16, v67
	v_lshlrev_b32_e32 v71, 16, v66
	v_add_f32_e32 v75, v75, v73
	v_add_f32_e32 v74, v74, v71
	v_exp_f32_e32 v73, v73
	v_exp_f32_e32 v71, v71
	v_and_b32_e32 v67, 0xffff0000, v67
	v_and_b32_e32 v66, 0xffff0000, v66
	v_fmac_f32_e32 v67, v73, v70
	v_lshlrev_b32_e32 v70, 16, v68
	v_fmac_f32_e32 v66, v71, v72
	v_lshlrev_b32_e32 v71, 16, v69
	v_add_f32_e32 v74, v74, v70
	v_exp_f32_e32 v76, v70
	v_add_f32_e32 v75, v75, v71
	v_exp_f32_e32 v77, v71
	ds_read2_b64 v[70:73], v237 offset0:108 offset1:126
	v_and_b32_e32 v68, 0xffff0000, v68
	v_fmac_f32_e32 v68, v76, v66
	v_and_b32_e32 v66, 0xffff0000, v69
	v_fmac_f32_e32 v66, v77, v67
	s_waitcnt lgkmcnt(0)
	v_lshlrev_b32_e32 v69, 16, v71
	v_lshlrev_b32_e32 v67, 16, v70
	v_add_f32_e32 v75, v75, v69
	v_add_f32_e32 v74, v74, v67
	v_exp_f32_e32 v69, v69
	v_exp_f32_e32 v67, v67
	v_and_b32_e32 v71, 0xffff0000, v71
	v_and_b32_e32 v70, 0xffff0000, v70
	v_fmac_f32_e32 v71, v69, v66
	v_lshlrev_b32_e32 v66, 16, v72
	v_fmac_f32_e32 v70, v67, v68
	v_lshlrev_b32_e32 v67, 16, v73
	v_add_f32_e32 v74, v74, v66
	v_exp_f32_e32 v76, v66
	v_add_f32_e32 v75, v75, v67
	v_exp_f32_e32 v77, v67
	ds_read2_b64 v[66:69], v237 offset0:144 offset1:162
	v_and_b32_e32 v72, 0xffff0000, v72
	v_fmac_f32_e32 v72, v76, v70
	v_and_b32_e32 v70, 0xffff0000, v73
	v_fmac_f32_e32 v70, v77, v71
	s_waitcnt lgkmcnt(0)
	v_lshlrev_b32_e32 v73, 16, v67
	v_lshlrev_b32_e32 v71, 16, v66
	v_add_f32_e32 v75, v75, v73
	v_add_f32_e32 v74, v74, v71
	v_exp_f32_e32 v73, v73
	v_exp_f32_e32 v71, v71
	v_and_b32_e32 v67, 0xffff0000, v67
	v_and_b32_e32 v66, 0xffff0000, v66
	v_fmac_f32_e32 v67, v73, v70
	v_lshlrev_b32_e32 v70, 16, v68
	v_fmac_f32_e32 v66, v71, v72
	v_lshlrev_b32_e32 v71, 16, v69
	v_add_f32_e32 v74, v74, v70
	v_exp_f32_e32 v76, v70
	v_add_f32_e32 v75, v75, v71
	v_exp_f32_e32 v77, v71
	ds_read2_b64 v[70:73], v237 offset0:180 offset1:198
	v_and_b32_e32 v68, 0xffff0000, v68
	v_fmac_f32_e32 v68, v76, v66
	v_and_b32_e32 v66, 0xffff0000, v69
	v_fmac_f32_e32 v66, v77, v67
	s_waitcnt lgkmcnt(0)
	v_lshlrev_b32_e32 v69, 16, v71
	v_lshlrev_b32_e32 v67, 16, v70
	v_add_f32_e32 v75, v75, v69
	v_add_f32_e32 v74, v74, v67
	v_exp_f32_e32 v69, v69
	v_exp_f32_e32 v67, v67
	v_and_b32_e32 v71, 0xffff0000, v71
	v_and_b32_e32 v70, 0xffff0000, v70
	v_fmac_f32_e32 v71, v69, v66
	v_lshlrev_b32_e32 v66, 16, v72
	v_fmac_f32_e32 v70, v67, v68
	v_lshlrev_b32_e32 v67, 16, v73
	v_add_f32_e32 v74, v74, v66
	v_exp_f32_e32 v76, v66
	v_add_f32_e32 v75, v75, v67
	v_exp_f32_e32 v77, v67
	ds_read2_b64 v[66:69], v237 offset0:216 offset1:234
	v_and_b32_e32 v72, 0xffff0000, v72
	v_fmac_f32_e32 v72, v76, v70
	v_and_b32_e32 v70, 0xffff0000, v73
	v_fmac_f32_e32 v70, v77, v71
	s_waitcnt lgkmcnt(0)
	v_lshlrev_b32_e32 v71, 16, v66
	v_lshlrev_b32_e32 v73, 16, v67
	v_add_f32_e32 v74, v74, v71
	v_add_f32_e32 v75, v75, v73
	v_exp_f32_e32 v71, v71
	v_exp_f32_e32 v73, v73
	v_and_b32_e32 v76, 0xffff0000, v66
	v_fmac_f32_e32 v76, v71, v72
	v_and_b32_e32 v71, 0xffff0000, v67
	v_lshlrev_b32_e32 v66, 16, v68
	v_fmac_f32_e32 v71, v73, v70
	v_lshlrev_b32_e32 v67, 16, v69
	v_add_f32_e32 v70, v74, v66
	v_exp_f32_e32 v73, v66
	v_add_f32_e32 v72, v75, v67
	v_and_b32_e32 v74, 0xffff0000, v68
	v_exp_f32_e32 v68, v67
	ds_read_b64 v[66:67], v237 offset:2016
	v_fmac_f32_e32 v74, v73, v76
	v_and_b32_e32 v73, 0xffff0000, v69
	v_fmac_f32_e32 v73, v68, v71
	ds_read_b64 v[68:69], v238
	s_waitcnt lgkmcnt(1)
	v_lshlrev_b32_e32 v71, 16, v66
	v_add_f32_e32 v70, v70, v71
	v_exp_f32_e32 v71, v71
	v_lshlrev_b32_e32 v75, 16, v67
	v_and_b32_e32 v66, 0xffff0000, v66
	v_add_f32_e32 v72, v72, v75
	v_fmac_f32_e32 v66, v71, v74
	s_waitcnt lgkmcnt(0)
	v_lshlrev_b32_e32 v71, 16, v68
	v_exp_f32_e32 v75, v75
	v_exp_f32_e32 v74, v71
	v_and_b32_e32 v67, 0xffff0000, v67
	v_fmac_f32_e32 v67, v75, v73
	v_lshlrev_b32_e32 v73, 16, v69
	v_add_f32_e32 v70, v70, v71
	v_and_b32_e32 v80, 0xffff0000, v68
	v_add_f32_e32 v71, v72, v73
	v_fmac_f32_e32 v80, v74, v66
	v_exp_f32_e32 v66, v73
	v_exp_f32_e32 v78, v70
	v_exp_f32_e32 v79, v71
	v_and_b32_e32 v81, 0xffff0000, v69
	v_fmac_f32_e32 v81, v66, v67
	ds_bpermute_b32 v66, v239, v78
	ds_bpermute_b32 v67, v239, v79
	ds_bpermute_b32 v68, v239, v80
	ds_bpermute_b32 v69, v239, v81
	ds_bpermute_b32 v70, v239, v78 offset:64
	ds_bpermute_b32 v71, v239, v79 offset:64
	ds_bpermute_b32 v72, v239, v80 offset:64
	ds_bpermute_b32 v73, v239, v81 offset:64
	ds_bpermute_b32 v74, v239, v78 offset:128
	ds_bpermute_b32 v75, v239, v79 offset:128
	ds_bpermute_b32 v76, v239, v80 offset:128
	ds_bpermute_b32 v77, v239, v81 offset:128
	ds_bpermute_b32 v78, v239, v78 offset:192
	ds_bpermute_b32 v79, v239, v79 offset:192
	ds_bpermute_b32 v80, v239, v80 offset:192
	ds_bpermute_b32 v81, v239, v81 offset:192
	s_and_saveexec_b64 s[48:49], s[0:1]
	s_cbranch_execz .LBB0_1280
	s_waitcnt lgkmcnt(10)
	v_pk_mul_f32 v[82:83], v[66:67], v[70:71]
	v_pk_fma_f32 v[66:67], v[66:67], 0, v[68:69] op_sel_hi:[1,0,1]
	v_mad_i64_i32 v[68:69], s[52:53], s81, v240, v[94:95]
	s_waitcnt lgkmcnt(8)
	v_pk_fma_f32 v[66:67], v[66:67], v[70:71], v[72:73]
	s_waitcnt lgkmcnt(6)
	v_pk_mul_f32 v[82:83], v[82:83], v[74:75]
	s_waitcnt lgkmcnt(4)
	v_pk_fma_f32 v[66:67], v[66:67], v[74:75], v[76:77]
	v_lshlrev_b64 v[68:69], 2, v[68:69]
	s_waitcnt lgkmcnt(2)
	v_pk_mul_f32 v[82:83], v[82:83], v[78:79]
	s_waitcnt lgkmcnt(0)
	v_pk_fma_f32 v[66:67], v[66:67], v[78:79], v[80:81]
	v_lshl_add_u64 v[70:71], s[8:9], 0, v[68:69]
	v_lshl_add_u64 v[68:69], s[10:11], 0, v[68:69]
	global_store_dwordx2 v[70:71], v[82:83], off
	global_store_dwordx2 v[68:69], v[66:67], off

.LBB0_1282:
	s_waitcnt lgkmcnt(12)
	ds_read_b128 v[66:69], v242
	s_waitcnt lgkmcnt(9)
	ds_read_b128 v[70:73], v242 offset:4096
	ds_read_b128 v[100:103], v242 offset:8192
	ds_read_b128 v[104:107], v242 offset:12288
	s_waitcnt vmcnt(15) lgkmcnt(3)
	v_mfma_f32_16x16x32_bf16 v[74:77], v[46:49], v[66:69], 0
	s_waitcnt vmcnt(9)
	v_mfma_f32_16x16x32_bf16 v[78:81], v[54:57], v[66:69], 0
	s_waitcnt vmcnt(8)
	v_mfma_f32_16x16x32_bf16 v[82:85], v[58:61], v[66:69], 0
	s_waitcnt vmcnt(3)
	v_mfma_f32_16x16x32_bf16 v[66:69], v[62:65], v[66:69], 0
	s_waitcnt lgkmcnt(2)
	v_mfma_f32_16x16x32_bf16 v[86:89], v[46:49], v[70:73], 0
	v_mfma_f32_16x16x32_bf16 v[90:93], v[54:57], v[70:73], 0
	v_mfma_f32_16x16x32_bf16 v[96:99], v[58:61], v[70:73], 0
	v_mfma_f32_16x16x32_bf16 v[70:73], v[62:65], v[70:73], 0
	s_waitcnt lgkmcnt(1)
	v_mfma_f32_16x16x32_bf16 v[108:111], v[46:49], v[100:103], 0
	v_mfma_f32_16x16x32_bf16 v[112:115], v[54:57], v[100:103], 0
	v_mfma_f32_16x16x32_bf16 v[120:123], v[58:61], v[100:103], 0
	v_mfma_f32_16x16x32_bf16 v[100:103], v[62:65], v[100:103], 0
	s_waitcnt lgkmcnt(0)
	v_mfma_f32_16x16x32_bf16 v[46:49], v[46:49], v[104:107], 0
	v_mfma_f32_16x16x32_bf16 v[54:57], v[54:57], v[104:107], 0
	v_mfma_f32_16x16x32_bf16 v[58:61], v[58:61], v[104:107], 0
	v_mfma_f32_16x16x32_bf16 v[62:65], v[62:65], v[104:107], 0
	ds_read_b128 v[104:107], v243
	ds_read_b128 v[124:127], v243 offset:4096
	s_waitcnt lgkmcnt(1)
	v_mfma_f32_16x16x32_bf16 v[74:77], v[30:33], v[104:107], v[74:77]
	v_mfma_f32_16x16x32_bf16 v[78:81], v[38:41], v[104:107], v[78:81]
	v_mfma_f32_16x16x32_bf16 v[82:85], v[42:45], v[104:107], v[82:85]
	s_waitcnt vmcnt(2)
	v_mfma_f32_16x16x32_bf16 v[66:69], v[50:53], v[104:107], v[66:69]
	s_waitcnt lgkmcnt(0)
	v_mfma_f32_16x16x32_bf16 v[86:89], v[30:33], v[124:127], v[86:89]
	v_mfma_f32_16x16x32_bf16 v[90:93], v[38:41], v[124:127], v[90:93]
	v_mfma_f32_16x16x32_bf16 v[96:99], v[42:45], v[124:127], v[96:99]
	v_mfma_f32_16x16x32_bf16 v[70:73], v[50:53], v[124:127], v[70:73]
	ds_read_b128 v[104:107], v243 offset:8192
	ds_read_b128 v[124:127], v243 offset:12288
	s_waitcnt lgkmcnt(1)
	v_mfma_f32_16x16x32_bf16 v[108:111], v[30:33], v[104:107], v[108:111]
	v_mfma_f32_16x16x32_bf16 v[112:115], v[38:41], v[104:107], v[112:115]
	v_mfma_f32_16x16x32_bf16 v[100:103], v[50:53], v[104:107], v[100:103]
	s_waitcnt lgkmcnt(0)
	v_mfma_f32_16x16x32_bf16 v[30:33], v[30:33], v[124:127], v[46:49]
	v_mfma_f32_16x16x32_bf16 v[38:41], v[38:41], v[124:127], v[54:57]
	v_mfma_f32_16x16x32_bf16 v[46:49], v[50:53], v[124:127], v[62:65]
	ds_read_b128 v[50:53], v244
	s_nop 0
	ds_read_b128 v[54:57], v244 offset:4096
	v_mfma_f32_16x16x32_bf16 v[120:123], v[42:45], v[104:107], v[120:123]
	v_mfma_f32_16x16x32_bf16 v[42:45], v[42:45], v[124:127], v[58:61]
	s_waitcnt lgkmcnt(1)
	v_mfma_f32_16x16x32_bf16 v[58:61], v[18:21], v[50:53], v[74:77]
	v_mfma_f32_16x16x32_bf16 v[62:65], v[22:25], v[50:53], v[78:81]
	v_mfma_f32_16x16x32_bf16 v[74:77], v[26:29], v[50:53], v[82:85]
	s_waitcnt vmcnt(1)
	v_mfma_f32_16x16x32_bf16 v[66:69], v[34:37], v[50:53], v[66:69]
	s_waitcnt lgkmcnt(0)
	v_mfma_f32_16x16x32_bf16 v[78:81], v[18:21], v[54:57], v[86:89]
	v_mfma_f32_16x16x32_bf16 v[104:107], v[22:25], v[54:57], v[90:93]
	v_mfma_f32_16x16x32_bf16 v[96:99], v[26:29], v[54:57], v[96:99]
	v_mfma_f32_16x16x32_bf16 v[70:73], v[34:37], v[54:57], v[70:73]
	ds_read_b128 v[50:53], v244 offset:8192
	ds_read_b128 v[54:57], v244 offset:12288
	s_waitcnt lgkmcnt(1)
	v_mfma_f32_16x16x32_bf16 v[108:111], v[18:21], v[50:53], v[108:111]
	s_waitcnt lgkmcnt(0)
	v_mfma_f32_16x16x32_bf16 v[124:127], v[18:21], v[54:57], v[30:33]
	ds_read_b128 v[18:21], v241
	s_nop 1
	ds_read_b128 v[30:33], v241 offset:4096
	v_mfma_f32_16x16x32_bf16 v[112:115], v[22:25], v[50:53], v[112:115]
	v_mfma_f32_16x16x32_bf16 v[128:131], v[22:25], v[54:57], v[38:41]
	v_add_co_u32_e32 v22, vcc, 0x1000, v174
	s_nop 1
	v_addc_co_u32_e32 v23, vcc, 0, v175, vcc
	v_add_co_u32_e32 v24, vcc, 0x1000, v172
	s_waitcnt lgkmcnt(1)
	v_mfma_f32_16x16x32_bf16 v[90:93], v[2:5], v[18:21], v[58:61]
	v_addc_co_u32_e32 v25, vcc, 0, v173, vcc
	v_mfma_f32_16x16x32_bf16 v[86:89], v[14:17], v[18:21], v[62:65]
	s_nop 0
	global_load_dwordx4 v[58:61], v[22:23], off offset:1024
	s_nop 0
	global_load_dwordx4 v[62:65], v[24:25], off offset:1024
	v_mfma_f32_16x16x32_bf16 v[120:123], v[26:29], v[50:53], v[120:123]
	v_mfma_f32_16x16x32_bf16 v[100:103], v[34:37], v[50:53], v[100:103]
	v_mfma_f32_16x16x32_bf16 v[136:139], v[34:37], v[54:57], v[46:49]
	v_mfma_f32_16x16x32_bf16 v[50:53], v[6:9], v[18:21], v[74:77]
	s_waitcnt vmcnt(2)
	v_mfma_f32_16x16x32_bf16 v[46:49], v[10:13], v[18:21], v[66:69]
	v_add_co_u32_e32 v18, vcc, 0x1000, v168
	s_nop 1
	v_addc_co_u32_e32 v19, vcc, 0, v169, vcc
	v_mfma_f32_16x16x32_bf16 v[132:135], v[26:29], v[54:57], v[42:45]
	global_load_dwordx4 v[54:57], v[18:19], off offset:1024
	global_load_dwordx4 v[26:29], v[22:23], off offset:1088
	s_nop 0
	global_load_dwordx4 v[22:25], v[24:25], off offset:1088
	s_nop 0
	global_load_dwordx4 v[18:21], v[18:19], off offset:1088
	s_waitcnt lgkmcnt(0)
	v_mfma_f32_16x16x32_bf16 v[82:85], v[2:5], v[30:33], v[78:81]
	v_mfma_f32_16x16x32_bf16 v[78:81], v[14:17], v[30:33], v[104:107]
	ds_read_b128 v[34:37], v241 offset:8192
	s_nop 1
	ds_read_b128 v[104:107], v241 offset:12288
	v_mfma_f32_16x16x32_bf16 v[42:45], v[6:9], v[30:33], v[96:99]
	v_mfma_f32_16x16x32_bf16 v[38:41], v[10:13], v[30:33], v[70:73]
	s_waitcnt vmcnt(5)
	v_pk_add_f32 v[30:31], v[58:59], v[90:91]
	s_nop 0
	v_pk_mul_f32 v[30:31], v[30:31], s[44:45] op_sel_hi:[1,0]
	s_waitcnt lgkmcnt(1)
	v_mfma_f32_16x16x32_bf16 v[70:73], v[2:5], v[34:37], v[108:111]
	s_waitcnt vmcnt(4)
	v_pk_add_f32 v[32:33], v[62:63], v[86:87]
	v_exp_f32_e32 v68, v30
	v_pk_mul_f32 v[66:67], v[32:33], s[44:45] op_sel_hi:[1,0]
	v_exp_f32_e32 v69, v31
	v_exp_f32_e32 v66, v66
	v_exp_f32_e32 v67, v67
	v_mfma_f32_16x16x32_bf16 v[74:77], v[14:17], v[34:37], v[112:115]
	v_add_f32_e64 v90, v68, 1.0
	v_add_f32_e64 v91, v69, 1.0
	ds_read_b64 v[86:87], v154
	v_pk_add_f32 v[96:97], v[66:67], 1.0 op_sel_hi:[1,0]
	v_mfma_f32_16x16x32_bf16 v[30:33], v[6:9], v[34:37], v[120:123]
	v_mul_f32_e64 v66, v90, v96
	v_mul_f32_e64 v67, v91, v97
	v_rcp_f32_e32 v98, v66
	v_rcp_f32_e32 v99, v67
	s_waitcnt lgkmcnt(1)
	v_mfma_f32_16x16x32_bf16 v[66:69], v[2:5], v[104:107], v[124:127]
	v_mul_f32_e64 v2, v96, v98
	v_mul_f32_e64 v3, v97, v99
	v_mfma_f32_16x16x32_bf16 v[34:37], v[10:13], v[34:37], v[100:103]
	s_waitcnt vmcnt(3)
	v_pk_mul_f32 v[96:97], v[54:55], v[2:3]
	s_nop 0
	v_pk_mul_f32 v[102:103], v[96:97], s[98:99] op_sel_hi:[1,0]
	v_mfma_f32_16x16x32_bf16 v[14:17], v[14:17], v[104:107], v[128:131]
	v_fma_f32 v2, v102, s46, v164
	v_fma_f32 v3, v103, s46, v164
	v_pk_fma_f32 v[100:101], v[102:103], v[2:3], 0.5 op_sel_hi:[1,1,0]
	v_mfma_f32_16x16x32_bf16 v[2:5], v[6:9], v[104:107], v[132:135]
	v_fma_f32 v6, v102, v100, 1.0
	v_fma_f32 v7, v103, v101, 1.0
	v_pk_mul_f32 v[100:101], v[6:7], v[102:103] neg_lo:[0,1] neg_hi:[0,1]
	v_min_f32_e32 v6, v102, v103
	v_cmp_ge_f32_e32 vcc, s66, v6
	v_mfma_f32_16x16x32_bf16 v[6:9], v[10:13], v[104:107], v[136:139]
	s_and_b64 vcc, exec, vcc
	s_cbranch_vccnz .LBB0_1324
.LBB0_1283:
	v_pk_add_f32 v[10:11], v[60:61], v[92:93]
	v_pk_add_f32 v[12:13], v[64:65], v[88:89]
	v_pk_mul_f32 v[10:11], v[10:11], s[44:45] op_sel_hi:[1,0]
	v_pk_mul_f32 v[12:13], v[12:13], s[44:45] op_sel_hi:[1,0]
	v_sqrt_f32_e32 v88, v100
	v_sqrt_f32_e32 v89, v101
	v_exp_f32_e32 v10, v10
	v_exp_f32_e32 v11, v11
	v_exp_f32_e32 v12, v12
	v_exp_f32_e32 v13, v13
	v_pk_mul_f32 v[90:91], v[90:91], v[98:99]
	s_waitcnt lgkmcnt(0)
	v_lshlrev_b32_e32 v92, 16, v86
	v_pk_mul_f32 v[98:99], v[90:91], v[88:89]
	v_pk_add_f32 v[88:89], v[10:11], 1.0 op_sel_hi:[1,0]
	v_pk_add_f32 v[12:13], v[12:13], 1.0 op_sel_hi:[1,0]
	v_and_b32_e32 v93, 0xffff0000, v86
	v_pk_mul_f32 v[10:11], v[88:89], v[12:13]
	s_nop 0
	v_rcp_f32_e32 v90, v10
	v_rcp_f32_e32 v91, v11
	v_pk_mul_f32 v[10:11], v[98:99], v[92:93]
	v_pk_mul_f32 v[12:13], v[12:13], v[90:91]
	s_nop 0
	v_pk_mul_f32 v[12:13], v[56:57], v[12:13]
	v_cvt_pk_bf16_f32 v10, v96, v10
	v_cvt_pk_bf16_f32 v11, v97, v11
	s_nop 0
	v_pk_mul_f32 v[96:97], v[12:13], s[98:99] op_sel_hi:[1,0]
	s_nop 0
	v_pk_fma_f32 v[92:93], v[96:97], s[46:47], v[164:165] op_sel_hi:[1,0,0]
	v_min_f32_e32 v86, v96, v97
	v_pk_fma_f32 v[92:93], v[96:97], v[92:93], 0.5 op_sel_hi:[1,1,0]
	v_cmp_ge_f32_e32 vcc, s66, v86
	v_pk_fma_f32 v[92:93], v[96:97], v[92:93], 1.0 op_sel_hi:[1,1,0]
	s_nop 0
	v_pk_mul_f32 v[92:93], v[92:93], v[96:97] neg_lo:[0,1] neg_hi:[0,1]
	s_and_b64 vcc, exec, vcc
	s_cbranch_vccnz .LBB0_1325
.LBB0_1284:
	v_pk_add_f32 v[82:83], v[58:59], v[82:83]
	v_pk_add_f32 v[78:79], v[62:63], v[78:79]
	v_sqrt_f32_e32 v92, v92
	v_sqrt_f32_e32 v93, v93
	v_pk_mul_f32 v[82:83], v[82:83], s[44:45] op_sel_hi:[1,0]
	v_pk_mul_f32 v[78:79], v[78:79], s[44:45] op_sel_hi:[1,0]
	v_pk_mul_f32 v[88:89], v[88:89], v[90:91]
	v_exp_f32_e32 v82, v82
	v_exp_f32_e32 v83, v83
	v_exp_f32_e32 v90, v78
	v_exp_f32_e32 v91, v79
	v_lshlrev_b32_e32 v86, 16, v87
	v_and_b32_e32 v87, 0xffff0000, v87
	v_pk_mul_f32 v[88:89], v[88:89], v[92:93]
	v_pk_add_f32 v[78:79], v[82:83], 1.0 op_sel_hi:[1,0]
	v_pk_mul_f32 v[86:87], v[88:89], v[86:87]
	v_pk_add_f32 v[88:89], v[90:91], 1.0 op_sel_hi:[1,0]
	v_cvt_pk_bf16_f32 v12, v12, v86
	v_cvt_pk_bf16_f32 v13, v13, v87
	ds_write_b128 v236, v[10:13]
	v_pk_mul_f32 v[82:83], v[78:79], v[88:89]
	ds_read_b64 v[12:13], v154 offset:4096
	v_rcp_f32_e32 v82, v82
	v_rcp_f32_e32 v83, v83
	s_nop 0
	v_pk_mul_f32 v[10:11], v[88:89], v[82:83]
	s_nop 0
	v_pk_mul_f32 v[10:11], v[54:55], v[10:11]
	s_nop 0
	v_pk_mul_f32 v[88:89], v[10:11], s[98:99] op_sel_hi:[1,0]
	s_nop 0
	v_pk_fma_f32 v[86:87], v[88:89], s[46:47], v[164:165] op_sel_hi:[1,0,0]
	v_min_f32_e32 v90, v88, v89
	v_pk_fma_f32 v[86:87], v[88:89], v[86:87], 0.5 op_sel_hi:[1,1,0]
	v_cmp_ge_f32_e32 vcc, s66, v90
	v_pk_fma_f32 v[86:87], v[88:89], v[86:87], 1.0 op_sel_hi:[1,1,0]
	s_nop 0
	v_pk_mul_f32 v[86:87], v[86:87], v[88:89] neg_lo:[0,1] neg_hi:[0,1]
	s_and_b64 vcc, exec, vcc
	s_cbranch_vccnz .LBB0_1326
.LBB0_1285:
	v_pk_add_f32 v[84:85], v[60:61], v[84:85]
	v_pk_add_f32 v[80:81], v[64:65], v[80:81]
	v_pk_mul_f32 v[84:85], v[84:85], s[44:45] op_sel_hi:[1,0]
	v_pk_mul_f32 v[80:81], v[80:81], s[44:45] op_sel_hi:[1,0]
	v_exp_f32_e32 v84, v84
	v_exp_f32_e32 v85, v85
	v_exp_f32_e32 v90, v80
	v_exp_f32_e32 v91, v81
	v_sqrt_f32_e32 v86, v86
	v_sqrt_f32_e32 v87, v87
	v_pk_add_f32 v[80:81], v[84:85], 1.0 op_sel_hi:[1,0]
	v_pk_add_f32 v[84:85], v[90:91], 1.0 op_sel_hi:[1,0]
	v_pk_mul_f32 v[78:79], v[78:79], v[82:83]
	v_pk_mul_f32 v[82:83], v[80:81], v[84:85]
	s_waitcnt lgkmcnt(0)
	v_lshlrev_b32_e32 v88, 16, v12
	v_rcp_f32_e32 v82, v82
	v_rcp_f32_e32 v83, v83
	v_and_b32_e32 v89, 0xffff0000, v12
	v_pk_mul_f32 v[78:79], v[78:79], v[86:87]
	s_nop 0
	v_pk_mul_f32 v[78:79], v[78:79], v[88:89]
	s_nop 0
	v_cvt_pk_bf16_f32 v10, v10, v78
	v_cvt_pk_bf16_f32 v11, v11, v79
	v_pk_mul_f32 v[78:79], v[84:85], v[82:83]
	s_nop 0
	v_pk_mul_f32 v[78:79], v[56:57], v[78:79]
	s_nop 0
	v_pk_mul_f32 v[84:85], v[78:79], s[98:99] op_sel_hi:[1,0]
	s_nop 0
	v_pk_fma_f32 v[86:87], v[84:85], s[46:47], v[164:165] op_sel_hi:[1,0,0]
	v_min_f32_e32 v12, v84, v85
	v_pk_fma_f32 v[86:87], v[84:85], v[86:87], 0.5 op_sel_hi:[1,1,0]
	v_cmp_ge_f32_e32 vcc, s66, v12
	v_pk_fma_f32 v[86:87], v[84:85], v[86:87], 1.0 op_sel_hi:[1,1,0]
	s_nop 0
	v_pk_mul_f32 v[86:87], v[86:87], v[84:85] neg_lo:[0,1] neg_hi:[0,1]
	s_and_b64 vcc, exec, vcc
	s_cbranch_vccnz .LBB0_1327
.LBB0_1286:
	v_pk_add_f32 v[70:71], v[58:59], v[70:71]
	v_pk_add_f32 v[74:75], v[62:63], v[74:75]
	v_sqrt_f32_e32 v84, v86
	v_sqrt_f32_e32 v85, v87
	v_pk_mul_f32 v[70:71], v[70:71], s[44:45] op_sel_hi:[1,0]
	v_pk_mul_f32 v[74:75], v[74:75], s[44:45] op_sel_hi:[1,0]
	v_exp_f32_e32 v70, v70
	v_exp_f32_e32 v71, v71
	v_exp_f32_e32 v74, v74
	v_exp_f32_e32 v75, v75
	v_pk_mul_f32 v[80:81], v[80:81], v[82:83]
	v_lshlrev_b32_e32 v12, 16, v13
	v_and_b32_e32 v13, 0xffff0000, v13
	v_pk_mul_f32 v[80:81], v[80:81], v[84:85]
	v_pk_add_f32 v[70:71], v[70:71], 1.0 op_sel_hi:[1,0]
	v_pk_mul_f32 v[12:13], v[80:81], v[12:13]
	v_pk_add_f32 v[80:81], v[74:75], 1.0 op_sel_hi:[1,0]
	v_cvt_pk_bf16_f32 v12, v78, v12
	v_cvt_pk_bf16_f32 v13, v79, v13
	ds_write_b128 v236, v[10:13] offset:2432
	v_pk_mul_f32 v[74:75], v[70:71], v[80:81]
	ds_read_b64 v[12:13], v154 offset:8192
	v_rcp_f32_e32 v74, v74
	v_rcp_f32_e32 v75, v75
	s_nop 0
	v_pk_mul_f32 v[10:11], v[80:81], v[74:75]
	s_nop 0
	v_pk_mul_f32 v[10:11], v[54:55], v[10:11]
	s_nop 0
	v_pk_mul_f32 v[80:81], v[10:11], s[98:99] op_sel_hi:[1,0]
	s_nop 0
	v_pk_fma_f32 v[78:79], v[80:81], s[46:47], v[164:165] op_sel_hi:[1,0,0]
	v_min_f32_e32 v82, v80, v81
	v_pk_fma_f32 v[78:79], v[80:81], v[78:79], 0.5 op_sel_hi:[1,1,0]
	v_cmp_ge_f32_e32 vcc, s66, v82
	v_pk_fma_f32 v[78:79], v[80:81], v[78:79], 1.0 op_sel_hi:[1,1,0]
	s_nop 0
	v_pk_mul_f32 v[78:79], v[78:79], v[80:81] neg_lo:[0,1] neg_hi:[0,1]
	s_and_b64 vcc, exec, vcc
	s_cbranch_vccnz .LBB0_1328
.LBB0_1287:
	v_pk_add_f32 v[72:73], v[60:61], v[72:73]
	v_pk_add_f32 v[76:77], v[64:65], v[76:77]
	v_pk_mul_f32 v[72:73], v[72:73], s[44:45] op_sel_hi:[1,0]
	v_pk_mul_f32 v[76:77], v[76:77], s[44:45] op_sel_hi:[1,0]
	v_exp_f32_e32 v72, v72
	v_exp_f32_e32 v73, v73
	v_exp_f32_e32 v76, v76
	v_exp_f32_e32 v77, v77
	v_sqrt_f32_e32 v78, v78
	v_sqrt_f32_e32 v79, v79
	v_pk_add_f32 v[72:73], v[72:73], 1.0 op_sel_hi:[1,0]
	v_pk_add_f32 v[76:77], v[76:77], 1.0 op_sel_hi:[1,0]
	v_pk_mul_f32 v[70:71], v[70:71], v[74:75]
	v_pk_mul_f32 v[74:75], v[72:73], v[76:77]
	s_waitcnt lgkmcnt(0)
	v_lshlrev_b32_e32 v80, 16, v12
	v_rcp_f32_e32 v74, v74
	v_rcp_f32_e32 v75, v75
	v_and_b32_e32 v81, 0xffff0000, v12
	v_pk_mul_f32 v[70:71], v[70:71], v[78:79]
	s_nop 0
	v_pk_mul_f32 v[70:71], v[70:71], v[80:81]
	s_nop 0
	v_cvt_pk_bf16_f32 v10, v10, v70
	v_cvt_pk_bf16_f32 v11, v11, v71
	v_pk_mul_f32 v[70:71], v[76:77], v[74:75]
	s_nop 0
	v_pk_mul_f32 v[70:71], v[56:57], v[70:71]
	s_nop 0
	v_pk_mul_f32 v[76:77], v[70:71], s[98:99] op_sel_hi:[1,0]
	s_nop 0
	v_pk_fma_f32 v[78:79], v[76:77], s[46:47], v[164:165] op_sel_hi:[1,0,0]
	v_min_f32_e32 v12, v76, v77
	v_pk_fma_f32 v[78:79], v[76:77], v[78:79], 0.5 op_sel_hi:[1,1,0]
	v_cmp_ge_f32_e32 vcc, s66, v12
	v_pk_fma_f32 v[78:79], v[76:77], v[78:79], 1.0 op_sel_hi:[1,1,0]
	s_nop 0
	v_pk_mul_f32 v[78:79], v[78:79], v[76:77] neg_lo:[0,1] neg_hi:[0,1]
	s_and_b64 vcc, exec, vcc
	s_cbranch_vccnz .LBB0_1329
.LBB0_1288:
	v_pk_add_f32 v[58:59], v[58:59], v[66:67]
	v_pk_add_f32 v[14:15], v[62:63], v[14:15]
	v_pk_mul_f32 v[58:59], v[58:59], s[44:45] op_sel_hi:[1,0]
	v_pk_mul_f32 v[14:15], v[14:15], s[44:45] op_sel_hi:[1,0]
	v_exp_f32_e32 v58, v58
	v_exp_f32_e32 v59, v59
	v_exp_f32_e32 v62, v14
	v_exp_f32_e32 v63, v15
	v_sqrt_f32_e32 v76, v78
	v_sqrt_f32_e32 v77, v79
	v_pk_add_f32 v[14:15], v[58:59], 1.0 op_sel_hi:[1,0]
	v_pk_add_f32 v[62:63], v[62:63], 1.0 op_sel_hi:[1,0]
	v_pk_mul_f32 v[72:73], v[72:73], v[74:75]
	v_pk_mul_f32 v[58:59], v[14:15], v[62:63]
	v_lshlrev_b32_e32 v12, 16, v13
	v_rcp_f32_e32 v58, v58
	v_rcp_f32_e32 v59, v59
	v_and_b32_e32 v13, 0xffff0000, v13
	v_pk_mul_f32 v[72:73], v[72:73], v[76:77]
	s_nop 0
	v_pk_mul_f32 v[12:13], v[72:73], v[12:13]
	s_nop 0
	v_cvt_pk_bf16_f32 v12, v70, v12
	v_cvt_pk_bf16_f32 v13, v71, v13
	ds_write_b128 v236, v[10:13] offset:4864
	v_pk_mul_f32 v[10:11], v[62:63], v[58:59]
	ds_read_b64 v[12:13], v154 offset:12288
	v_pk_mul_f32 v[10:11], v[54:55], v[10:11]
	s_nop 0
	v_pk_mul_f32 v[62:63], v[10:11], s[98:99] op_sel_hi:[1,0]
	s_nop 0
	v_pk_fma_f32 v[54:55], v[62:63], s[46:47], v[164:165] op_sel_hi:[1,0,0]
	v_min_f32_e32 v66, v62, v63
	v_pk_fma_f32 v[54:55], v[62:63], v[54:55], 0.5 op_sel_hi:[1,1,0]
	v_cmp_ge_f32_e32 vcc, s66, v66
	v_pk_fma_f32 v[54:55], v[62:63], v[54:55], 1.0 op_sel_hi:[1,1,0]
	s_nop 0
	v_pk_mul_f32 v[54:55], v[54:55], v[62:63] neg_lo:[0,1] neg_hi:[0,1]
	s_and_b64 vcc, exec, vcc
	s_cbranch_vccnz .LBB0_1330
.LBB0_1289:
	v_pk_add_f32 v[60:61], v[60:61], v[68:69]
	v_pk_add_f32 v[16:17], v[64:65], v[16:17]
	v_pk_mul_f32 v[60:61], v[60:61], s[44:45] op_sel_hi:[1,0]
	v_pk_mul_f32 v[16:17], v[16:17], s[44:45] op_sel_hi:[1,0]
	v_sqrt_f32_e32 v54, v54
	v_sqrt_f32_e32 v55, v55
	v_exp_f32_e32 v60, v60
	v_exp_f32_e32 v61, v61
	v_exp_f32_e32 v16, v16
	v_exp_f32_e32 v17, v17
	v_pk_mul_f32 v[14:15], v[14:15], v[58:59]
	s_waitcnt lgkmcnt(0)
	v_lshlrev_b32_e32 v62, 16, v12
	v_pk_mul_f32 v[54:55], v[14:15], v[54:55]
	v_pk_add_f32 v[14:15], v[60:61], 1.0 op_sel_hi:[1,0]
	v_pk_add_f32 v[58:59], v[16:17], 1.0 op_sel_hi:[1,0]
	v_and_b32_e32 v63, 0xffff0000, v12
	v_pk_mul_f32 v[16:17], v[14:15], v[58:59]
	v_pk_mul_f32 v[54:55], v[54:55], v[62:63]
	v_rcp_f32_e32 v16, v16
	v_rcp_f32_e32 v17, v17
	v_cvt_pk_bf16_f32 v10, v10, v54
	v_cvt_pk_bf16_f32 v11, v11, v55
	s_nop 0
	v_pk_mul_f32 v[54:55], v[58:59], v[16:17]
	s_nop 0
	v_pk_mul_f32 v[54:55], v[56:57], v[54:55]
	s_nop 0
	v_pk_mul_f32 v[56:57], v[54:55], s[98:99] op_sel_hi:[1,0]
	s_nop 0
	v_pk_fma_f32 v[58:59], v[56:57], s[46:47], v[164:165] op_sel_hi:[1,0,0]
	v_min_f32_e32 v12, v56, v57
	v_pk_fma_f32 v[58:59], v[56:57], v[58:59], 0.5 op_sel_hi:[1,1,0]
	v_cmp_ge_f32_e32 vcc, s66, v12
	v_pk_fma_f32 v[58:59], v[56:57], v[58:59], 1.0 op_sel_hi:[1,1,0]
	s_nop 0
	v_pk_mul_f32 v[58:59], v[58:59], v[56:57] neg_lo:[0,1] neg_hi:[0,1]
	s_and_b64 vcc, exec, vcc
	s_cbranch_vccnz .LBB0_1331
.LBB0_1290:
	v_pk_mul_f32 v[14:15], v[14:15], v[16:17]
	s_waitcnt vmcnt(2)
	v_pk_add_f32 v[16:17], v[26:27], v[50:51]
	s_waitcnt vmcnt(1)
	v_pk_add_f32 v[46:47], v[22:23], v[46:47]
	v_sqrt_f32_e32 v56, v58
	v_sqrt_f32_e32 v57, v59
	v_pk_mul_f32 v[16:17], v[16:17], s[44:45] op_sel_hi:[1,0]
	v_pk_mul_f32 v[46:47], v[46:47], s[44:45] op_sel_hi:[1,0]
	v_exp_f32_e32 v16, v16
	v_exp_f32_e32 v17, v17
	v_exp_f32_e32 v46, v46
	v_exp_f32_e32 v47, v47
	v_lshlrev_b32_e32 v12, 16, v13
	v_and_b32_e32 v13, 0xffff0000, v13
	v_pk_mul_f32 v[14:15], v[14:15], v[56:57]
	v_pk_add_f32 v[46:47], v[46:47], 1.0 op_sel_hi:[1,0]
	v_pk_mul_f32 v[12:13], v[14:15], v[12:13]
	v_pk_add_f32 v[14:15], v[16:17], 1.0 op_sel_hi:[1,0]
	v_cvt_pk_bf16_f32 v12, v54, v12
	v_cvt_pk_bf16_f32 v13, v55, v13
	ds_write_b128 v236, v[10:13] offset:7296
	v_pk_mul_f32 v[16:17], v[14:15], v[46:47]
	ds_read_b64 v[12:13], v118
	v_rcp_f32_e32 v16, v16
	v_rcp_f32_e32 v17, v17
	s_nop 0
	v_pk_mul_f32 v[10:11], v[46:47], v[16:17]
	s_waitcnt vmcnt(0)
	v_pk_mul_f32 v[10:11], v[18:19], v[10:11]
	s_nop 0
	v_pk_mul_f32 v[50:51], v[10:11], s[98:99] op_sel_hi:[1,0]
	s_nop 0
	v_pk_fma_f32 v[46:47], v[50:51], s[46:47], v[164:165] op_sel_hi:[1,0,0]
	v_min_f32_e32 v54, v50, v51
	v_pk_fma_f32 v[46:47], v[50:51], v[46:47], 0.5 op_sel_hi:[1,1,0]
	v_cmp_ge_f32_e32 vcc, s66, v54
	v_pk_fma_f32 v[46:47], v[50:51], v[46:47], 1.0 op_sel_hi:[1,1,0]
	s_nop 0
	v_pk_mul_f32 v[46:47], v[46:47], v[50:51] neg_lo:[0,1] neg_hi:[0,1]
	s_and_b64 vcc, exec, vcc
	s_cbranch_vccnz .LBB0_1332
.LBB0_1291:
	v_pk_add_f32 v[50:51], v[28:29], v[52:53]
	v_pk_add_f32 v[48:49], v[24:25], v[48:49]
	v_pk_mul_f32 v[50:51], v[50:51], s[44:45] op_sel_hi:[1,0]
	v_pk_mul_f32 v[48:49], v[48:49], s[44:45] op_sel_hi:[1,0]
	v_sqrt_f32_e32 v46, v46
	v_sqrt_f32_e32 v47, v47
	v_exp_f32_e32 v50, v50
	v_exp_f32_e32 v51, v51
	v_exp_f32_e32 v48, v48
	v_exp_f32_e32 v49, v49
	v_pk_mul_f32 v[14:15], v[14:15], v[16:17]
	s_waitcnt lgkmcnt(0)
	v_lshlrev_b32_e32 v52, 16, v12
	v_pk_mul_f32 v[16:17], v[14:15], v[46:47]
	v_pk_add_f32 v[14:15], v[50:51], 1.0 op_sel_hi:[1,0]
	v_pk_add_f32 v[48:49], v[48:49], 1.0 op_sel_hi:[1,0]
	v_and_b32_e32 v53, 0xffff0000, v12
	v_pk_mul_f32 v[46:47], v[14:15], v[48:49]
	v_pk_mul_f32 v[16:17], v[16:17], v[52:53]
	v_rcp_f32_e32 v46, v46
	v_rcp_f32_e32 v47, v47
	v_cvt_pk_bf16_f32 v10, v10, v16
	v_cvt_pk_bf16_f32 v11, v11, v17
	s_nop 0
	v_pk_mul_f32 v[16:17], v[48:49], v[46:47]
	s_nop 0
	v_pk_mul_f32 v[16:17], v[20:21], v[16:17]
	s_nop 0
	v_pk_mul_f32 v[50:51], v[16:17], s[98:99] op_sel_hi:[1,0]
	s_nop 0
	v_pk_fma_f32 v[48:49], v[50:51], s[46:47], v[164:165] op_sel_hi:[1,0,0]
	v_min_f32_e32 v12, v50, v51
	v_pk_fma_f32 v[48:49], v[50:51], v[48:49], 0.5 op_sel_hi:[1,1,0]
	v_cmp_ge_f32_e32 vcc, s66, v12
	v_pk_fma_f32 v[48:49], v[50:51], v[48:49], 1.0 op_sel_hi:[1,1,0]
	s_nop 0
	v_pk_mul_f32 v[48:49], v[48:49], v[50:51] neg_lo:[0,1] neg_hi:[0,1]
	s_and_b64 vcc, exec, vcc
	s_cbranch_vccnz .LBB0_1333
.LBB0_1292:
	v_pk_add_f32 v[42:43], v[26:27], v[42:43]
	v_pk_add_f32 v[38:39], v[22:23], v[38:39]
	v_sqrt_f32_e32 v48, v48
	v_sqrt_f32_e32 v49, v49
	v_pk_mul_f32 v[42:43], v[42:43], s[44:45] op_sel_hi:[1,0]
	v_pk_mul_f32 v[38:39], v[38:39], s[44:45] op_sel_hi:[1,0]
	v_exp_f32_e32 v42, v42
	v_exp_f32_e32 v43, v43
	v_exp_f32_e32 v38, v38
	v_exp_f32_e32 v39, v39
	v_pk_mul_f32 v[14:15], v[14:15], v[46:47]
	v_lshlrev_b32_e32 v12, 16, v13
	v_and_b32_e32 v13, 0xffff0000, v13
	v_pk_mul_f32 v[14:15], v[14:15], v[48:49]
	s_nop 0
	v_pk_mul_f32 v[12:13], v[14:15], v[12:13]
	v_pk_add_f32 v[14:15], v[42:43], 1.0 op_sel_hi:[1,0]
	v_pk_add_f32 v[42:43], v[38:39], 1.0 op_sel_hi:[1,0]
	v_cvt_pk_bf16_f32 v12, v16, v12
	v_cvt_pk_bf16_f32 v13, v17, v13
	ds_write_b128 v236, v[10:13] offset:64
	v_pk_mul_f32 v[38:39], v[14:15], v[42:43]
	ds_read_b64 v[12:13], v118 offset:4096
	v_rcp_f32_e32 v38, v38
	v_rcp_f32_e32 v39, v39
	s_nop 0
	v_pk_mul_f32 v[10:11], v[42:43], v[38:39]
	s_nop 0
	v_pk_mul_f32 v[10:11], v[18:19], v[10:11]
	s_nop 0
	v_pk_mul_f32 v[42:43], v[10:11], s[98:99] op_sel_hi:[1,0]
	s_nop 0
	v_pk_fma_f32 v[16:17], v[42:43], s[46:47], v[164:165] op_sel_hi:[1,0,0]
	v_min_f32_e32 v46, v42, v43
	v_pk_fma_f32 v[16:17], v[42:43], v[16:17], 0.5 op_sel_hi:[1,1,0]
	v_cmp_ge_f32_e32 vcc, s66, v46
	v_pk_fma_f32 v[16:17], v[42:43], v[16:17], 1.0 op_sel_hi:[1,1,0]
	s_nop 0
	v_pk_mul_f32 v[16:17], v[16:17], v[42:43] neg_lo:[0,1] neg_hi:[0,1]
	s_and_b64 vcc, exec, vcc
	s_cbranch_vccnz .LBB0_1334
.LBB0_1293:
	v_pk_add_f32 v[42:43], v[28:29], v[44:45]
	v_pk_add_f32 v[40:41], v[24:25], v[40:41]
	v_pk_mul_f32 v[42:43], v[42:43], s[44:45] op_sel_hi:[1,0]
	v_pk_mul_f32 v[40:41], v[40:41], s[44:45] op_sel_hi:[1,0]
	v_sqrt_f32_e32 v16, v16
	v_sqrt_f32_e32 v17, v17
	v_exp_f32_e32 v42, v42
	v_exp_f32_e32 v43, v43
	v_exp_f32_e32 v40, v40
	v_exp_f32_e32 v41, v41
	v_pk_mul_f32 v[14:15], v[14:15], v[38:39]
	s_waitcnt lgkmcnt(0)
	v_lshlrev_b32_e32 v44, 16, v12
	v_pk_mul_f32 v[38:39], v[14:15], v[16:17]
	v_pk_add_f32 v[14:15], v[42:43], 1.0 op_sel_hi:[1,0]
	v_pk_add_f32 v[40:41], v[40:41], 1.0 op_sel_hi:[1,0]
	v_and_b32_e32 v45, 0xffff0000, v12
	v_pk_mul_f32 v[16:17], v[14:15], v[40:41]
	v_pk_mul_f32 v[38:39], v[38:39], v[44:45]
	v_rcp_f32_e32 v16, v16
	v_rcp_f32_e32 v17, v17
	v_cvt_pk_bf16_f32 v10, v10, v38
	v_cvt_pk_bf16_f32 v11, v11, v39
	s_nop 0
	v_pk_mul_f32 v[38:39], v[40:41], v[16:17]
	s_nop 0
	v_pk_mul_f32 v[38:39], v[20:21], v[38:39]
	s_nop 0
	v_pk_mul_f32 v[40:41], v[38:39], s[98:99] op_sel_hi:[1,0]
	s_nop 0
	v_pk_fma_f32 v[42:43], v[40:41], s[46:47], v[164:165] op_sel_hi:[1,0,0]
	v_min_f32_e32 v12, v40, v41
	v_pk_fma_f32 v[42:43], v[40:41], v[42:43], 0.5 op_sel_hi:[1,1,0]
	v_cmp_ge_f32_e32 vcc, s66, v12
	v_pk_fma_f32 v[42:43], v[40:41], v[42:43], 1.0 op_sel_hi:[1,1,0]
	s_nop 0
	v_pk_mul_f32 v[42:43], v[42:43], v[40:41] neg_lo:[0,1] neg_hi:[0,1]
	s_and_b64 vcc, exec, vcc
	s_cbranch_vccnz .LBB0_1335
.LBB0_1294:
	v_pk_mul_f32 v[14:15], v[14:15], v[16:17]
	v_pk_add_f32 v[16:17], v[26:27], v[30:31]
	v_pk_add_f32 v[30:31], v[22:23], v[34:35]
	v_sqrt_f32_e32 v40, v42
	v_sqrt_f32_e32 v41, v43
	v_pk_mul_f32 v[16:17], v[16:17], s[44:45] op_sel_hi:[1,0]
	v_pk_mul_f32 v[30:31], v[30:31], s[44:45] op_sel_hi:[1,0]
	v_exp_f32_e32 v16, v16
	v_exp_f32_e32 v17, v17
	v_exp_f32_e32 v30, v30
	v_exp_f32_e32 v31, v31
	v_lshlrev_b32_e32 v12, 16, v13
	v_and_b32_e32 v13, 0xffff0000, v13
	v_pk_mul_f32 v[14:15], v[14:15], v[40:41]
	v_pk_add_f32 v[30:31], v[30:31], 1.0 op_sel_hi:[1,0]
	v_pk_mul_f32 v[12:13], v[14:15], v[12:13]
	v_pk_add_f32 v[14:15], v[16:17], 1.0 op_sel_hi:[1,0]
	v_cvt_pk_bf16_f32 v12, v38, v12
	v_cvt_pk_bf16_f32 v13, v39, v13
	ds_write_b128 v236, v[10:13] offset:2496
	v_pk_mul_f32 v[16:17], v[14:15], v[30:31]
	ds_read_b64 v[12:13], v118 offset:8192
	v_rcp_f32_e32 v16, v16
	v_rcp_f32_e32 v17, v17
	s_nop 0
	v_pk_mul_f32 v[10:11], v[30:31], v[16:17]
	s_nop 0
	v_pk_mul_f32 v[10:11], v[18:19], v[10:11]
	s_nop 0
	v_pk_mul_f32 v[34:35], v[10:11], s[98:99] op_sel_hi:[1,0]
	s_nop 0
	v_pk_fma_f32 v[30:31], v[34:35], s[46:47], v[164:165] op_sel_hi:[1,0,0]
	v_min_f32_e32 v38, v34, v35
	v_pk_fma_f32 v[30:31], v[34:35], v[30:31], 0.5 op_sel_hi:[1,1,0]
	v_cmp_ge_f32_e32 vcc, s66, v38
	v_pk_fma_f32 v[30:31], v[34:35], v[30:31], 1.0 op_sel_hi:[1,1,0]
	s_nop 0
	v_pk_mul_f32 v[30:31], v[30:31], v[34:35] neg_lo:[0,1] neg_hi:[0,1]
	s_and_b64 vcc, exec, vcc
	s_cbranch_vccnz .LBB0_1336
.LBB0_1295:
	v_pk_add_f32 v[32:33], v[28:29], v[32:33]
	v_pk_add_f32 v[34:35], v[24:25], v[36:37]
	v_pk_mul_f32 v[32:33], v[32:33], s[44:45] op_sel_hi:[1,0]
	v_pk_mul_f32 v[34:35], v[34:35], s[44:45] op_sel_hi:[1,0]
	v_sqrt_f32_e32 v30, v30
	v_sqrt_f32_e32 v31, v31
	v_exp_f32_e32 v32, v32
	v_exp_f32_e32 v33, v33
	v_exp_f32_e32 v34, v34
	v_exp_f32_e32 v35, v35
	v_pk_mul_f32 v[14:15], v[14:15], v[16:17]
	s_waitcnt lgkmcnt(0)
	v_lshlrev_b32_e32 v36, 16, v12
	v_pk_mul_f32 v[16:17], v[14:15], v[30:31]
	v_pk_add_f32 v[14:15], v[32:33], 1.0 op_sel_hi:[1,0]
	v_pk_add_f32 v[32:33], v[34:35], 1.0 op_sel_hi:[1,0]
	v_and_b32_e32 v37, 0xffff0000, v12
	v_pk_mul_f32 v[30:31], v[14:15], v[32:33]
	v_pk_mul_f32 v[16:17], v[16:17], v[36:37]
	v_rcp_f32_e32 v30, v30
	v_rcp_f32_e32 v31, v31
	v_cvt_pk_bf16_f32 v10, v10, v16
	v_cvt_pk_bf16_f32 v11, v11, v17
	s_nop 0
	v_pk_mul_f32 v[16:17], v[32:33], v[30:31]
	s_nop 0
	v_pk_mul_f32 v[16:17], v[20:21], v[16:17]
	s_nop 0
	v_pk_mul_f32 v[32:33], v[16:17], s[98:99] op_sel_hi:[1,0]
	s_nop 0
	v_pk_fma_f32 v[34:35], v[32:33], s[46:47], v[164:165] op_sel_hi:[1,0,0]
	v_min_f32_e32 v12, v32, v33
	v_pk_fma_f32 v[34:35], v[32:33], v[34:35], 0.5 op_sel_hi:[1,1,0]
	v_cmp_ge_f32_e32 vcc, s66, v12
	v_pk_fma_f32 v[34:35], v[32:33], v[34:35], 1.0 op_sel_hi:[1,1,0]
	s_nop 0
	v_pk_mul_f32 v[34:35], v[34:35], v[32:33] neg_lo:[0,1] neg_hi:[0,1]
	s_and_b64 vcc, exec, vcc
	s_cbranch_vccnz .LBB0_1337
.LBB0_1296:
	v_pk_add_f32 v[2:3], v[26:27], v[2:3]
	v_pk_add_f32 v[6:7], v[22:23], v[6:7]
	v_pk_mul_f32 v[2:3], v[2:3], s[44:45] op_sel_hi:[1,0]
	v_pk_mul_f32 v[6:7], v[6:7], s[44:45] op_sel_hi:[1,0]
	v_exp_f32_e32 v2, v2
	v_exp_f32_e32 v3, v3
	v_exp_f32_e32 v6, v6
	v_exp_f32_e32 v7, v7
	v_sqrt_f32_e32 v32, v34
	v_sqrt_f32_e32 v33, v35
	v_pk_mul_f32 v[14:15], v[14:15], v[30:31]
	v_pk_add_f32 v[2:3], v[2:3], 1.0 op_sel_hi:[1,0]
	v_pk_add_f32 v[22:23], v[6:7], 1.0 op_sel_hi:[1,0]
	v_lshlrev_b32_e32 v12, 16, v13
	v_and_b32_e32 v13, 0xffff0000, v13
	v_pk_mul_f32 v[14:15], v[14:15], v[32:33]
	v_pk_mul_f32 v[6:7], v[2:3], v[22:23]
	v_pk_mul_f32 v[12:13], v[14:15], v[12:13]
	v_rcp_f32_e32 v14, v6
	v_rcp_f32_e32 v15, v7
	v_cvt_pk_bf16_f32 v12, v16, v12
	v_cvt_pk_bf16_f32 v13, v17, v13
	ds_write_b128 v236, v[10:13] offset:4928
	v_pk_mul_f32 v[10:11], v[22:23], v[14:15]
	ds_read_b64 v[6:7], v118 offset:12288
	v_pk_mul_f32 v[10:11], v[18:19], v[10:11]
	s_nop 0
	v_pk_mul_f32 v[16:17], v[10:11], s[98:99] op_sel_hi:[1,0]
	s_nop 0
	v_pk_fma_f32 v[12:13], v[16:17], s[46:47], v[164:165] op_sel_hi:[1,0,0]
	v_min_f32_e32 v18, v16, v17
	v_pk_fma_f32 v[12:13], v[16:17], v[12:13], 0.5 op_sel_hi:[1,1,0]
	v_cmp_ge_f32_e32 vcc, s66, v18
	v_pk_fma_f32 v[12:13], v[16:17], v[12:13], 1.0 op_sel_hi:[1,1,0]
	s_nop 0
	v_pk_mul_f32 v[12:13], v[12:13], v[16:17] neg_lo:[0,1] neg_hi:[0,1]
	s_and_b64 vcc, exec, vcc
	s_cbranch_vccnz .LBB0_1338
.LBB0_1297:
	v_pk_add_f32 v[4:5], v[28:29], v[4:5]
	v_pk_add_f32 v[8:9], v[24:25], v[8:9]
	v_pk_mul_f32 v[4:5], v[4:5], s[44:45] op_sel_hi:[1,0]
	v_pk_mul_f32 v[8:9], v[8:9], s[44:45] op_sel_hi:[1,0]
	v_exp_f32_e32 v4, v4
	v_exp_f32_e32 v5, v5
	v_exp_f32_e32 v18, v8
	v_exp_f32_e32 v19, v9
	v_sqrt_f32_e32 v12, v12
	v_sqrt_f32_e32 v13, v13
	v_pk_mul_f32 v[2:3], v[2:3], v[14:15]
	v_pk_add_f32 v[8:9], v[4:5], 1.0 op_sel_hi:[1,0]
	v_pk_add_f32 v[4:5], v[18:19], 1.0 op_sel_hi:[1,0]
	v_pk_mul_f32 v[2:3], v[2:3], v[12:13]
	v_pk_mul_f32 v[12:13], v[8:9], v[4:5]
	s_waitcnt lgkmcnt(0)
	v_lshlrev_b32_e32 v16, 16, v6
	v_rcp_f32_e32 v12, v12
	v_rcp_f32_e32 v13, v13
	v_and_b32_e32 v17, 0xffff0000, v6
	v_pk_mul_f32 v[2:3], v[2:3], v[16:17]
	v_pk_mul_f32 v[4:5], v[4:5], v[12:13]
	s_nop 0
	v_pk_mul_f32 v[4:5], v[20:21], v[4:5]
	v_cvt_pk_bf16_f32 v2, v10, v2
	v_cvt_pk_bf16_f32 v3, v11, v3
	s_nop 0
	v_pk_mul_f32 v[14:15], v[4:5], s[98:99] op_sel_hi:[1,0]
	s_nop 0
	v_pk_fma_f32 v[10:11], v[14:15], s[46:47], v[164:165] op_sel_hi:[1,0,0]
	v_min_f32_e32 v6, v14, v15
	v_pk_fma_f32 v[10:11], v[14:15], v[10:11], 0.5 op_sel_hi:[1,1,0]
	v_cmp_ge_f32_e32 vcc, s66, v6
	v_pk_fma_f32 v[10:11], v[14:15], v[10:11], 1.0 op_sel_hi:[1,1,0]
	s_nop 0
	v_pk_mul_f32 v[10:11], v[10:11], v[14:15] neg_lo:[0,1] neg_hi:[0,1]
	s_and_b64 vcc, exec, vcc
	s_cbranch_vccnz .LBB0_1339
.LBB0_1298:
	v_sqrt_f32_e32 v10, v10
	v_sqrt_f32_e32 v11, v11
	s_add_i32 s80, s80, s28
	s_cmpk_gt_i32 s80, 0xb3f
	v_pk_mul_f32 v[8:9], v[8:9], v[12:13]
	s_cselect_b64 s[52:53], -1, 0
	v_lshlrev_b32_e32 v6, 16, v7
	v_and_b32_e32 v7, 0xffff0000, v7
	v_pk_mul_f32 v[8:9], v[8:9], v[10:11]
	s_and_b64 vcc, exec, s[52:53]
	v_pk_mul_f32 v[6:7], v[8:9], v[6:7]
	s_nop 0
	v_cvt_pk_bf16_f32 v4, v4, v6
	v_cvt_pk_bf16_f32 v5, v5, v7
	ds_write_b128 v236, v[2:5] offset:7360
	s_cbranch_vccnz .LBB0_1304
	s_mul_hi_i32 s20, s80, 0x66666667
	s_lshr_b32 s54, s20, 31
	s_ashr_i32 s20, s20, 2
	s_add_i32 s56, s20, s54
	s_cmpk_lt_i32 s80, 0xa00
	s_cselect_b64 s[54:55], -1, 0
	s_mov_b64 s[60:61], -1
	s_and_b64 vcc, exec, s[54:55]
	s_cbranch_vccnz .LBB0_1301
	s_add_i32 s20, s56, 0xffffff00
	s_lshl_b64 s[58:59], s[20:21], 7
	s_add_u32 s58, s58, 0x8000
	s_addc_u32 s59, s59, 0
	s_mov_b64 s[60:61], 0

.LBB0_1308:
	s_and_saveexec_b64 s[52:53], vcc
	v_mul_f32_e32 v170, 0x3fb8aa3b, v182
	v_exp_f32_e32 v180, v170
	v_mul_f32_e32 v170, 0x3fb8aa3b, v183
	v_exp_f32_e32 v181, v170
	s_nop 0
	v_pk_add_f32 v[180:181], v[180:181], 1.0 op_sel_hi:[1,0] neg_lo:[1,0] neg_hi:[1,0]
	s_or_b64 exec, exec, s[52:53]
	s_branch .LBB0_1263
.LBB0_1309:
	s_and_saveexec_b64 s[52:53], vcc
	v_mul_f32_e32 v150, 0x3fb8aa3b, v180
	v_exp_f32_e32 v176, v150
	v_mul_f32_e32 v150, 0x3fb8aa3b, v181
	v_exp_f32_e32 v177, v150
	s_nop 0
	v_pk_add_f32 v[176:177], v[176:177], 1.0 op_sel_hi:[1,0] neg_lo:[1,0] neg_hi:[1,0]
	s_or_b64 exec, exec, s[52:53]
	s_branch .LBB0_1264
.LBB0_1310:
	s_and_saveexec_b64 s[52:53], vcc
	v_mul_f32_e32 v148, 0x3fb8aa3b, v152
	v_mul_f32_e32 v149, 0x3fb8aa3b, v153
	v_exp_f32_e32 v148, v148
	v_exp_f32_e32 v149, v149
	s_nop 0
	v_pk_add_f32 v[148:149], v[148:149], 1.0 op_sel_hi:[1,0] neg_lo:[1,0] neg_hi:[1,0]
	s_or_b64 exec, exec, s[52:53]
	s_branch .LBB0_1265
.LBB0_1311:
	s_and_saveexec_b64 s[52:53], vcc
	v_mul_f32_e32 v142, 0x3fb8aa3b, v146
	v_exp_f32_e32 v146, v142
	v_mul_f32_e32 v142, 0x3fb8aa3b, v147
	v_exp_f32_e32 v147, v142
	s_nop 0
	v_pk_add_f32 v[150:151], v[146:147], 1.0 op_sel_hi:[1,0] neg_lo:[1,0] neg_hi:[1,0]
	s_or_b64 exec, exec, s[52:53]
	s_branch .LBB0_1266
.LBB0_1312:
	s_and_saveexec_b64 s[52:53], vcc
	v_mul_f32_e32 v140, 0x3fb8aa3b, v144
	v_mul_f32_e32 v141, 0x3fb8aa3b, v145
	v_exp_f32_e32 v140, v140
	v_exp_f32_e32 v141, v141
	s_nop 0
	v_pk_add_f32 v[140:141], v[140:141], 1.0 op_sel_hi:[1,0] neg_lo:[1,0] neg_hi:[1,0]
	s_or_b64 exec, exec, s[52:53]
	s_branch .LBB0_1267
.LBB0_1313:
	s_and_saveexec_b64 s[52:53], vcc
	v_mul_f32_e32 v134, 0x3fb8aa3b, v138
	v_exp_f32_e32 v138, v134
	v_mul_f32_e32 v134, 0x3fb8aa3b, v139
	v_exp_f32_e32 v139, v134
	s_nop 0
	v_pk_add_f32 v[142:143], v[138:139], 1.0 op_sel_hi:[1,0] neg_lo:[1,0] neg_hi:[1,0]
	s_or_b64 exec, exec, s[52:53]
	s_branch .LBB0_1268
.LBB0_1314:
	s_and_saveexec_b64 s[52:53], vcc
	v_mul_f32_e32 v126, 0x3fb8aa3b, v130
	v_mul_f32_e32 v127, 0x3fb8aa3b, v131
	v_exp_f32_e32 v126, v126
	v_exp_f32_e32 v127, v127
	s_nop 0
	v_pk_add_f32 v[126:127], v[126:127], 1.0 op_sel_hi:[1,0] neg_lo:[1,0] neg_hi:[1,0]
	s_or_b64 exec, exec, s[52:53]
	s_branch .LBB0_1269
.LBB0_1315:
	s_and_saveexec_b64 s[52:53], vcc
	v_mul_f32_e32 v114, 0x3fb8aa3b, v120
	v_exp_f32_e32 v120, v114
	v_mul_f32_e32 v114, 0x3fb8aa3b, v121
	v_exp_f32_e32 v121, v114
	s_nop 0
	v_pk_add_f32 v[122:123], v[120:121], 1.0 op_sel_hi:[1,0] neg_lo:[1,0] neg_hi:[1,0]
	s_or_b64 exec, exec, s[52:53]
	s_branch .LBB0_1270
.LBB0_1316:
	s_and_saveexec_b64 s[52:53], vcc
	v_mul_f32_e32 v114, 0x3fb8aa3b, v116
	v_mul_f32_e32 v115, 0x3fb8aa3b, v117
	v_exp_f32_e32 v114, v114
	v_exp_f32_e32 v115, v115
	s_nop 0
	v_pk_add_f32 v[114:115], v[114:115], 1.0 op_sel_hi:[1,0] neg_lo:[1,0] neg_hi:[1,0]
	s_or_b64 exec, exec, s[52:53]
	s_branch .LBB0_1271
.LBB0_1317:
	s_and_saveexec_b64 s[52:53], vcc
	v_mul_f32_e32 v106, 0x3fb8aa3b, v114
	v_exp_f32_e32 v110, v106
	v_mul_f32_e32 v106, 0x3fb8aa3b, v115
	v_exp_f32_e32 v111, v106
	s_nop 0
	v_pk_add_f32 v[110:111], v[110:111], 1.0 op_sel_hi:[1,0] neg_lo:[1,0] neg_hi:[1,0]
	s_or_b64 exec, exec, s[52:53]
	s_branch .LBB0_1272
.LBB0_1318:
	s_and_saveexec_b64 s[52:53], vcc
	v_mul_f32_e32 v104, 0x3fb8aa3b, v108
	v_mul_f32_e32 v105, 0x3fb8aa3b, v109
	v_exp_f32_e32 v104, v104
	v_exp_f32_e32 v105, v105
	s_nop 0
	v_pk_add_f32 v[104:105], v[104:105], 1.0 op_sel_hi:[1,0] neg_lo:[1,0] neg_hi:[1,0]
	s_or_b64 exec, exec, s[52:53]
	s_branch .LBB0_1273
.LBB0_1319:
	s_and_saveexec_b64 s[52:53], vcc
	v_mul_f32_e32 v98, 0x3fb8aa3b, v102
	v_exp_f32_e32 v102, v98
	v_mul_f32_e32 v98, 0x3fb8aa3b, v103
	v_exp_f32_e32 v103, v98
	s_nop 0
	v_pk_add_f32 v[106:107], v[102:103], 1.0 op_sel_hi:[1,0] neg_lo:[1,0] neg_hi:[1,0]
	s_or_b64 exec, exec, s[52:53]
	s_branch .LBB0_1274
.LBB0_1320:
	s_and_saveexec_b64 s[52:53], vcc
	v_mul_f32_e32 v96, 0x3fb8aa3b, v100
	v_mul_f32_e32 v97, 0x3fb8aa3b, v101
	v_exp_f32_e32 v96, v96
	v_exp_f32_e32 v97, v97
	s_nop 0
	v_pk_add_f32 v[96:97], v[96:97], 1.0 op_sel_hi:[1,0] neg_lo:[1,0] neg_hi:[1,0]
	s_or_b64 exec, exec, s[52:53]
	s_branch .LBB0_1275
.LBB0_1321:
	s_and_saveexec_b64 s[52:53], vcc
	v_mul_f32_e32 v90, 0x3fb8aa3b, v94
	v_exp_f32_e32 v94, v90
	v_mul_f32_e32 v90, 0x3fb8aa3b, v95
	v_exp_f32_e32 v95, v90
	s_nop 0
	v_pk_add_f32 v[98:99], v[94:95], 1.0 op_sel_hi:[1,0] neg_lo:[1,0] neg_hi:[1,0]
	s_or_b64 exec, exec, s[52:53]
	s_branch .LBB0_1276
.LBB0_1322:
	s_and_saveexec_b64 s[52:53], vcc
	v_mul_f32_e32 v82, 0x3fb8aa3b, v86
	v_mul_f32_e32 v83, 0x3fb8aa3b, v87
	v_exp_f32_e32 v82, v82
	v_exp_f32_e32 v83, v83
	s_nop 0
	v_pk_add_f32 v[82:83], v[82:83], 1.0 op_sel_hi:[1,0] neg_lo:[1,0] neg_hi:[1,0]
	s_or_b64 exec, exec, s[52:53]
	s_branch .LBB0_1277
.LBB0_1323:
	s_and_saveexec_b64 s[52:53], vcc
	v_mul_f32_e32 v70, 0x3fb8aa3b, v78
	v_exp_f32_e32 v76, v70
	v_mul_f32_e32 v70, 0x3fb8aa3b, v79
	v_exp_f32_e32 v77, v70
	s_nop 0
	v_pk_add_f32 v[76:77], v[76:77], 1.0 op_sel_hi:[1,0] neg_lo:[1,0] neg_hi:[1,0]
	s_or_b64 exec, exec, s[52:53]
	s_branch .LBB0_1278
.LBB0_1324:
	s_and_saveexec_b64 s[52:53], vcc
	v_mul_f32_e32 v10, 0x3fb8aa3b, v102
	v_mul_f32_e32 v11, 0x3fb8aa3b, v103
	v_exp_f32_e32 v10, v10
	v_exp_f32_e32 v11, v11
	s_nop 0
	v_pk_add_f32 v[100:101], v[10:11], 1.0 op_sel_hi:[1,0] neg_lo:[1,0] neg_hi:[1,0]
	s_or_b64 exec, exec, s[52:53]
	s_branch .LBB0_1283
.LBB0_1325:
	s_and_saveexec_b64 s[52:53], vcc
	v_mul_f32_e32 v86, 0x3fb8aa3b, v96
	v_exp_f32_e32 v92, v86
	v_mul_f32_e32 v86, 0x3fb8aa3b, v97
	v_exp_f32_e32 v93, v86
	s_nop 0
	v_pk_add_f32 v[92:93], v[92:93], 1.0 op_sel_hi:[1,0] neg_lo:[1,0] neg_hi:[1,0]
	s_or_b64 exec, exec, s[52:53]
	s_branch .LBB0_1284
.LBB0_1326:
	s_and_saveexec_b64 s[52:53], vcc
	v_mul_f32_e32 v86, 0x3fb8aa3b, v88
	v_mul_f32_e32 v87, 0x3fb8aa3b, v89
	v_exp_f32_e32 v86, v86
	v_exp_f32_e32 v87, v87
	s_nop 0
	v_pk_add_f32 v[86:87], v[86:87], 1.0 op_sel_hi:[1,0] neg_lo:[1,0] neg_hi:[1,0]
	s_or_b64 exec, exec, s[52:53]
	s_branch .LBB0_1285
.LBB0_1327:
	s_and_saveexec_b64 s[52:53], vcc
	v_mul_f32_e32 v12, 0x3fb8aa3b, v84
	v_exp_f32_e32 v84, v12
	v_mul_f32_e32 v12, 0x3fb8aa3b, v85
	v_exp_f32_e32 v85, v12
	s_nop 0
	v_pk_add_f32 v[86:87], v[84:85], 1.0 op_sel_hi:[1,0] neg_lo:[1,0] neg_hi:[1,0]
	s_or_b64 exec, exec, s[52:53]
	s_branch .LBB0_1286
.LBB0_1328:
	s_and_saveexec_b64 s[52:53], vcc
	v_mul_f32_e32 v78, 0x3fb8aa3b, v80
	v_mul_f32_e32 v79, 0x3fb8aa3b, v81
	v_exp_f32_e32 v78, v78
	v_exp_f32_e32 v79, v79
	s_nop 0
	v_pk_add_f32 v[78:79], v[78:79], 1.0 op_sel_hi:[1,0] neg_lo:[1,0] neg_hi:[1,0]
	s_or_b64 exec, exec, s[52:53]
	s_branch .LBB0_1287
.LBB0_1329:
	s_and_saveexec_b64 s[52:53], vcc
	v_mul_f32_e32 v12, 0x3fb8aa3b, v76
	v_exp_f32_e32 v76, v12
	v_mul_f32_e32 v12, 0x3fb8aa3b, v77
	v_exp_f32_e32 v77, v12
	s_nop 0
	v_pk_add_f32 v[78:79], v[76:77], 1.0 op_sel_hi:[1,0] neg_lo:[1,0] neg_hi:[1,0]
	s_or_b64 exec, exec, s[52:53]
	s_branch .LBB0_1288
.LBB0_1330:
	s_and_saveexec_b64 s[52:53], vcc
	v_mul_f32_e32 v54, 0x3fb8aa3b, v62
	v_mul_f32_e32 v55, 0x3fb8aa3b, v63
	v_exp_f32_e32 v54, v54
	v_exp_f32_e32 v55, v55
	s_nop 0
	v_pk_add_f32 v[54:55], v[54:55], 1.0 op_sel_hi:[1,0] neg_lo:[1,0] neg_hi:[1,0]
	s_or_b64 exec, exec, s[52:53]
	s_branch .LBB0_1289
.LBB0_1331:
	s_and_saveexec_b64 s[52:53], vcc
	v_mul_f32_e32 v12, 0x3fb8aa3b, v56
	v_exp_f32_e32 v56, v12
	v_mul_f32_e32 v12, 0x3fb8aa3b, v57
	v_exp_f32_e32 v57, v12
	s_nop 0
	v_pk_add_f32 v[58:59], v[56:57], 1.0 op_sel_hi:[1,0] neg_lo:[1,0] neg_hi:[1,0]
	s_or_b64 exec, exec, s[52:53]
	s_branch .LBB0_1290
.LBB0_1332:
	s_and_saveexec_b64 s[52:53], vcc
	v_mul_f32_e32 v46, 0x3fb8aa3b, v50
	v_mul_f32_e32 v47, 0x3fb8aa3b, v51
	v_exp_f32_e32 v46, v46
	v_exp_f32_e32 v47, v47
	s_nop 0
	v_pk_add_f32 v[46:47], v[46:47], 1.0 op_sel_hi:[1,0] neg_lo:[1,0] neg_hi:[1,0]
	s_or_b64 exec, exec, s[52:53]
	s_branch .LBB0_1291
.LBB0_1333:
	s_and_saveexec_b64 s[52:53], vcc
	v_mul_f32_e32 v12, 0x3fb8aa3b, v50
	v_exp_f32_e32 v48, v12
	v_mul_f32_e32 v12, 0x3fb8aa3b, v51
	v_exp_f32_e32 v49, v12
	s_nop 0
	v_pk_add_f32 v[48:49], v[48:49], 1.0 op_sel_hi:[1,0] neg_lo:[1,0] neg_hi:[1,0]
	s_or_b64 exec, exec, s[52:53]
	s_branch .LBB0_1292
.LBB0_1334:
	s_and_saveexec_b64 s[52:53], vcc
	v_mul_f32_e32 v16, 0x3fb8aa3b, v42
	v_mul_f32_e32 v17, 0x3fb8aa3b, v43
	v_exp_f32_e32 v16, v16
	v_exp_f32_e32 v17, v17
	s_nop 0
	v_pk_add_f32 v[16:17], v[16:17], 1.0 op_sel_hi:[1,0] neg_lo:[1,0] neg_hi:[1,0]
	s_or_b64 exec, exec, s[52:53]
	s_branch .LBB0_1293
.LBB0_1335:
	s_and_saveexec_b64 s[52:53], vcc
	v_mul_f32_e32 v12, 0x3fb8aa3b, v40
	v_exp_f32_e32 v40, v12
	v_mul_f32_e32 v12, 0x3fb8aa3b, v41
	v_exp_f32_e32 v41, v12
	s_nop 0
	v_pk_add_f32 v[42:43], v[40:41], 1.0 op_sel_hi:[1,0] neg_lo:[1,0] neg_hi:[1,0]
	s_or_b64 exec, exec, s[52:53]
	s_branch .LBB0_1294
.LBB0_1336:
	s_and_saveexec_b64 s[52:53], vcc
	v_mul_f32_e32 v30, 0x3fb8aa3b, v34
	v_mul_f32_e32 v31, 0x3fb8aa3b, v35
	v_exp_f32_e32 v30, v30
	v_exp_f32_e32 v31, v31
	s_nop 0
	v_pk_add_f32 v[30:31], v[30:31], 1.0 op_sel_hi:[1,0] neg_lo:[1,0] neg_hi:[1,0]
	s_or_b64 exec, exec, s[52:53]
	s_branch .LBB0_1295
.LBB0_1337:
	s_and_saveexec_b64 s[52:53], vcc
	v_mul_f32_e32 v12, 0x3fb8aa3b, v32
	v_exp_f32_e32 v32, v12
	v_mul_f32_e32 v12, 0x3fb8aa3b, v33
	v_exp_f32_e32 v33, v12
	s_nop 0
	v_pk_add_f32 v[34:35], v[32:33], 1.0 op_sel_hi:[1,0] neg_lo:[1,0] neg_hi:[1,0]
	s_or_b64 exec, exec, s[52:53]
	s_branch .LBB0_1296
.LBB0_1338:
	s_and_saveexec_b64 s[52:53], vcc
	v_mul_f32_e32 v12, 0x3fb8aa3b, v16
	v_mul_f32_e32 v13, 0x3fb8aa3b, v17
	v_exp_f32_e32 v12, v12
	v_exp_f32_e32 v13, v13
	s_nop 0
	v_pk_add_f32 v[12:13], v[12:13], 1.0 op_sel_hi:[1,0] neg_lo:[1,0] neg_hi:[1,0]
	s_or_b64 exec, exec, s[52:53]
	s_branch .LBB0_1297
.LBB0_1339:
	s_and_saveexec_b64 s[52:53], vcc
	v_mul_f32_e32 v6, 0x3fb8aa3b, v14
	v_exp_f32_e32 v10, v6
	v_mul_f32_e32 v6, 0x3fb8aa3b, v15
	v_exp_f32_e32 v11, v6
	s_nop 0
	v_pk_add_f32 v[10:11], v[10:11], 1.0 op_sel_hi:[1,0] neg_lo:[1,0] neg_hi:[1,0]
	s_or_b64 exec, exec, s[52:53]
	s_branch .LBB0_1298
